# norm2 router: the 128 LDS weight reads per pass issued 3 reads ahead of their FMAs into rotating registers (was read -> lgkmcnt(0) -> FMA, serialized)
# speedup vs baseline: 1.0098x; 1.0086x over previous
; #define LAS __attribute__((address_space(3)))
; __device__ __forceinline__ void phase_norm2(const Params& p, const Ctx& F, const int l) {
;     ...
;         unsigned wro = (unsigned)(uintptr_t)wr; asm volatile("" : "+v"(wro));
;         const LAS float* wr2 = (const LAS float*)(uintptr_t)wro;
; #pragma unroll
;         for (int e = 0; e < 16; ++e) { f32x2 a = {0.f, 0.f};
; #pragma unroll
;             for (int j = 0; j < 8; ++j) { const f32x4 w = *((const LAS f32x4*)(wr2 + e * DM) + F.lane + 64 * j);
; #pragma unroll
;                 for (int c = 0; c < 4; ++c) a += vv[j][c] * w[c]; }
;             lg[e] = a; }
.LBB0_937:
	s_or_b64 exec, exec, s[12:13]
	v_mov_b32_e32 v1, v35
	s_nop 0
	v_lshl_add_u32 v182, v132, 4, v1
	v_add_u32_e32 v244, 0x10000, v182
	ds_read_b128 v[224:227], v182
	ds_read_b128 v[228:231], v182 offset:1024
	ds_read_b128 v[232:235], v182 offset:2048
	ds_read_b128 v[236:239], v182 offset:3072
	s_waitcnt lgkmcnt(3)
	v_pk_fma_f32 v[156:157], v[124:125], v[224:225], 0 op_sel_hi:[1,0,0]
	s_nop 0
	v_pk_fma_f32 v[152:153], v[126:127], v[224:225], v[156:157] op_sel:[0,1,0]
	s_nop 0
	v_pk_fma_f32 v[152:153], v[128:129], v[226:227], v[152:153] op_sel_hi:[1,0,1]
	v_mov_b32_e32 v154, v227
	v_pk_fma_f32 v[156:157], v[130:131], v[154:155], v[152:153] op_sel_hi:[1,0,1]
	ds_read_b128 v[240:243], v182 offset:4096
	s_waitcnt lgkmcnt(3)
	v_pk_fma_f32 v[156:157], v[112:113], v[228:229], v[156:157] op_sel_hi:[1,0,1]
	s_nop 0
	v_pk_fma_f32 v[152:153], v[114:115], v[228:229], v[156:157] op_sel:[0,1,0]
	s_nop 0
	v_pk_fma_f32 v[152:153], v[118:119], v[230:231], v[152:153] op_sel_hi:[1,0,1]
	v_mov_b32_e32 v154, v231
	v_pk_fma_f32 v[156:157], v[122:123], v[154:155], v[152:153] op_sel_hi:[1,0,1]
	ds_read_b128 v[224:227], v182 offset:5120
	s_waitcnt lgkmcnt(3)
	v_pk_fma_f32 v[156:157], v[108:109], v[232:233], v[156:157] op_sel_hi:[1,0,1]
	s_nop 0
	v_pk_fma_f32 v[152:153], v[110:111], v[232:233], v[156:157] op_sel:[0,1,0]
	s_nop 0
	v_pk_fma_f32 v[152:153], v[116:117], v[234:235], v[152:153] op_sel_hi:[1,0,1]
	v_mov_b32_e32 v154, v235
	v_pk_fma_f32 v[156:157], v[120:121], v[154:155], v[152:153] op_sel_hi:[1,0,1]
	ds_read_b128 v[228:231], v182 offset:6144
	s_waitcnt lgkmcnt(3)
	v_pk_fma_f32 v[156:157], v[96:97], v[236:237], v[156:157] op_sel_hi:[1,0,1]
	s_nop 0
	v_pk_fma_f32 v[152:153], v[98:99], v[236:237], v[156:157] op_sel:[0,1,0]
	s_nop 0
	v_pk_fma_f32 v[152:153], v[102:103], v[238:239], v[152:153] op_sel_hi:[1,0,1]
	v_mov_b32_e32 v154, v239
	v_pk_fma_f32 v[156:157], v[106:107], v[154:155], v[152:153] op_sel_hi:[1,0,1]
	ds_read_b128 v[232:235], v182 offset:7168
	s_waitcnt lgkmcnt(3)
	v_pk_fma_f32 v[156:157], v[92:93], v[240:241], v[156:157] op_sel_hi:[1,0,1]
	s_nop 0
	v_pk_fma_f32 v[152:153], v[94:95], v[240:241], v[156:157] op_sel:[0,1,0]
	s_nop 0
	v_pk_fma_f32 v[152:153], v[100:101], v[242:243], v[152:153] op_sel_hi:[1,0,1]
	v_mov_b32_e32 v154, v243
	v_pk_fma_f32 v[156:157], v[104:105], v[154:155], v[152:153] op_sel_hi:[1,0,1]
	ds_read_b128 v[236:239], v182 offset:8192
	s_waitcnt lgkmcnt(3)
	v_pk_fma_f32 v[156:157], v[80:81], v[224:225], v[156:157] op_sel_hi:[1,0,1]
	s_nop 0
	v_pk_fma_f32 v[152:153], v[82:83], v[224:225], v[156:157] op_sel:[0,1,0]
	s_nop 0
	v_pk_fma_f32 v[152:153], v[86:87], v[226:227], v[152:153] op_sel_hi:[1,0,1]
	v_mov_b32_e32 v154, v227
	v_pk_fma_f32 v[156:157], v[90:91], v[154:155], v[152:153] op_sel_hi:[1,0,1]
	ds_read_b128 v[240:243], v182 offset:9216
	s_waitcnt lgkmcnt(3)
	v_pk_fma_f32 v[156:157], v[76:77], v[228:229], v[156:157] op_sel_hi:[1,0,1]
	s_nop 0
	v_pk_fma_f32 v[152:153], v[78:79], v[228:229], v[156:157] op_sel:[0,1,0]
	s_nop 0
	v_pk_fma_f32 v[152:153], v[84:85], v[230:231], v[152:153] op_sel_hi:[1,0,1]
	v_mov_b32_e32 v154, v231
	v_pk_fma_f32 v[156:157], v[88:89], v[154:155], v[152:153] op_sel_hi:[1,0,1]
	ds_read_b128 v[224:227], v182 offset:10240
	s_waitcnt lgkmcnt(3)
	v_pk_fma_f32 v[156:157], v[68:69], v[232:233], v[156:157] op_sel_hi:[1,0,1]
	s_nop 0
	v_pk_fma_f32 v[152:153], v[70:71], v[232:233], v[156:157] op_sel:[0,1,0]
	s_nop 0
	v_pk_fma_f32 v[152:153], v[72:73], v[234:235], v[152:153] op_sel_hi:[1,0,1]
	v_mov_b32_e32 v154, v235
	v_pk_fma_f32 v[152:153], v[74:75], v[154:155], v[152:153] op_sel_hi:[1,0,1]
	ds_read_b128 v[228:231], v182 offset:11264
	s_waitcnt lgkmcnt(3)
	v_pk_fma_f32 v[158:159], v[124:125], v[236:237], 0 op_sel_hi:[1,0,0]
	s_nop 0
	v_pk_fma_f32 v[154:155], v[126:127], v[236:237], v[158:159] op_sel:[0,1,0]
	s_nop 0
	v_pk_fma_f32 v[154:155], v[128:129], v[238:239], v[154:155] op_sel_hi:[1,0,1]
	v_mov_b32_e32 v156, v239
	v_pk_fma_f32 v[158:159], v[130:131], v[156:157], v[154:155] op_sel_hi:[1,0,1]
	ds_read_b128 v[232:235], v182 offset:12288
	s_waitcnt lgkmcnt(3)
	v_pk_fma_f32 v[158:159], v[112:113], v[240:241], v[158:159] op_sel_hi:[1,0,1]
	s_nop 0
	v_pk_fma_f32 v[154:155], v[114:115], v[240:241], v[158:159] op_sel:[0,1,0]
	s_nop 0
	v_pk_fma_f32 v[154:155], v[118:119], v[242:243], v[154:155] op_sel_hi:[1,0,1]
	v_mov_b32_e32 v156, v243
	v_pk_fma_f32 v[158:159], v[122:123], v[156:157], v[154:155] op_sel_hi:[1,0,1]
	ds_read_b128 v[236:239], v182 offset:13312
	s_waitcnt lgkmcnt(3)
	v_pk_fma_f32 v[158:159], v[108:109], v[224:225], v[158:159] op_sel_hi:[1,0,1]
	s_nop 0
	v_pk_fma_f32 v[154:155], v[110:111], v[224:225], v[158:159] op_sel:[0,1,0]
	s_nop 0
	v_pk_fma_f32 v[154:155], v[116:117], v[226:227], v[154:155] op_sel_hi:[1,0,1]
	v_mov_b32_e32 v156, v227
	v_pk_fma_f32 v[158:159], v[120:121], v[156:157], v[154:155] op_sel_hi:[1,0,1]
	ds_read_b128 v[240:243], v182 offset:14336
	s_waitcnt lgkmcnt(3)
	v_pk_fma_f32 v[158:159], v[96:97], v[228:229], v[158:159] op_sel_hi:[1,0,1]
	s_nop 0
	v_pk_fma_f32 v[154:155], v[98:99], v[228:229], v[158:159] op_sel:[0,1,0]
	s_nop 0
	v_pk_fma_f32 v[154:155], v[102:103], v[230:231], v[154:155] op_sel_hi:[1,0,1]
	v_mov_b32_e32 v156, v231
	v_pk_fma_f32 v[158:159], v[106:107], v[156:157], v[154:155] op_sel_hi:[1,0,1]
	ds_read_b128 v[224:227], v182 offset:15360
	s_waitcnt lgkmcnt(3)
	v_pk_fma_f32 v[158:159], v[92:93], v[232:233], v[158:159] op_sel_hi:[1,0,1]
	s_nop 0
	v_pk_fma_f32 v[154:155], v[94:95], v[232:233], v[158:159] op_sel:[0,1,0]
	s_nop 0
	v_pk_fma_f32 v[154:155], v[100:101], v[234:235], v[154:155] op_sel_hi:[1,0,1]
	v_mov_b32_e32 v156, v235
	v_pk_fma_f32 v[158:159], v[104:105], v[156:157], v[154:155] op_sel_hi:[1,0,1]
	ds_read_b128 v[228:231], v182 offset:16384
	s_waitcnt lgkmcnt(3)
; #define LAS __attribute__((address_space(3)))
; __device__ __forceinline__ void phase_norm2(const Params& p, const Ctx& F, const int l) {
;     ...
;         unsigned wro = (unsigned)(uintptr_t)wr; asm volatile("" : "+v"(wro));
;         const LAS float* wr2 = (const LAS float*)(uintptr_t)wro;
; #pragma unroll
;         for (int e = 0; e < 16; ++e) { f32x2 a = {0.f, 0.f};
; #pragma unroll
;             for (int j = 0; j < 8; ++j) { const f32x4 w = *((const LAS f32x4*)(wr2 + e * DM) + F.lane + 64 * j);
; #pragma unroll
;                 for (int c = 0; c < 4; ++c) a += vv[j][c] * w[c]; }
;             lg[e] = a; }
	v_pk_fma_f32 v[158:159], v[80:81], v[236:237], v[158:159] op_sel_hi:[1,0,1]
	s_nop 0
	v_pk_fma_f32 v[154:155], v[82:83], v[236:237], v[158:159] op_sel:[0,1,0]
	s_nop 0
	v_pk_fma_f32 v[154:155], v[86:87], v[238:239], v[154:155] op_sel_hi:[1,0,1]
	v_mov_b32_e32 v156, v239
	v_pk_fma_f32 v[158:159], v[90:91], v[156:157], v[154:155] op_sel_hi:[1,0,1]
	ds_read_b128 v[232:235], v182 offset:17408
	s_waitcnt lgkmcnt(3)
	v_pk_fma_f32 v[158:159], v[76:77], v[240:241], v[158:159] op_sel_hi:[1,0,1]
	s_nop 0
	v_pk_fma_f32 v[154:155], v[78:79], v[240:241], v[158:159] op_sel:[0,1,0]
	s_nop 0
	v_pk_fma_f32 v[154:155], v[84:85], v[242:243], v[154:155] op_sel_hi:[1,0,1]
	v_mov_b32_e32 v156, v243
	v_pk_fma_f32 v[158:159], v[88:89], v[156:157], v[154:155] op_sel_hi:[1,0,1]
	ds_read_b128 v[236:239], v182 offset:18432
	s_waitcnt lgkmcnt(3)
	v_pk_fma_f32 v[158:159], v[68:69], v[224:225], v[158:159] op_sel_hi:[1,0,1]
	s_nop 0
	v_pk_fma_f32 v[154:155], v[70:71], v[224:225], v[158:159] op_sel:[0,1,0]
	s_nop 0
	v_pk_fma_f32 v[154:155], v[72:73], v[226:227], v[154:155] op_sel_hi:[1,0,1]
	v_mov_b32_e32 v156, v227
	v_pk_fma_f32 v[154:155], v[74:75], v[156:157], v[154:155] op_sel_hi:[1,0,1]
	ds_read_b128 v[240:243], v182 offset:19456
	s_waitcnt lgkmcnt(3)
	v_pk_fma_f32 v[160:161], v[124:125], v[228:229], 0 op_sel_hi:[1,0,0]
	s_nop 0
	v_pk_fma_f32 v[156:157], v[126:127], v[228:229], v[160:161] op_sel:[0,1,0]
	s_nop 0
	v_pk_fma_f32 v[156:157], v[128:129], v[230:231], v[156:157] op_sel_hi:[1,0,1]
	v_mov_b32_e32 v158, v231
	v_pk_fma_f32 v[160:161], v[130:131], v[158:159], v[156:157] op_sel_hi:[1,0,1]
	ds_read_b128 v[224:227], v182 offset:20480
	s_waitcnt lgkmcnt(3)
	v_pk_fma_f32 v[160:161], v[112:113], v[232:233], v[160:161] op_sel_hi:[1,0,1]
	s_nop 0
	v_pk_fma_f32 v[156:157], v[114:115], v[232:233], v[160:161] op_sel:[0,1,0]
	s_nop 0
	v_pk_fma_f32 v[156:157], v[118:119], v[234:235], v[156:157] op_sel_hi:[1,0,1]
	v_mov_b32_e32 v158, v235
	v_pk_fma_f32 v[160:161], v[122:123], v[158:159], v[156:157] op_sel_hi:[1,0,1]
	ds_read_b128 v[228:231], v182 offset:21504
	s_waitcnt lgkmcnt(3)
	v_pk_fma_f32 v[160:161], v[108:109], v[236:237], v[160:161] op_sel_hi:[1,0,1]
	s_nop 0
	v_pk_fma_f32 v[156:157], v[110:111], v[236:237], v[160:161] op_sel:[0,1,0]
	s_nop 0
	v_pk_fma_f32 v[156:157], v[116:117], v[238:239], v[156:157] op_sel_hi:[1,0,1]
	v_mov_b32_e32 v158, v239
	v_pk_fma_f32 v[160:161], v[120:121], v[158:159], v[156:157] op_sel_hi:[1,0,1]
	ds_read_b128 v[232:235], v182 offset:22528
	s_waitcnt lgkmcnt(3)
	v_pk_fma_f32 v[160:161], v[96:97], v[240:241], v[160:161] op_sel_hi:[1,0,1]
	s_nop 0
	v_pk_fma_f32 v[156:157], v[98:99], v[240:241], v[160:161] op_sel:[0,1,0]
	s_nop 0
	v_pk_fma_f32 v[156:157], v[102:103], v[242:243], v[156:157] op_sel_hi:[1,0,1]
	v_mov_b32_e32 v158, v243
	v_pk_fma_f32 v[160:161], v[106:107], v[158:159], v[156:157] op_sel_hi:[1,0,1]
	ds_read_b128 v[236:239], v182 offset:23552
	s_waitcnt lgkmcnt(3)
	v_pk_fma_f32 v[160:161], v[92:93], v[224:225], v[160:161] op_sel_hi:[1,0,1]
	s_nop 0
	v_pk_fma_f32 v[156:157], v[94:95], v[224:225], v[160:161] op_sel:[0,1,0]
	s_nop 0
	v_pk_fma_f32 v[156:157], v[100:101], v[226:227], v[156:157] op_sel_hi:[1,0,1]
	v_mov_b32_e32 v158, v227
	v_pk_fma_f32 v[160:161], v[104:105], v[158:159], v[156:157] op_sel_hi:[1,0,1]
	ds_read_b128 v[240:243], v182 offset:24576
	s_waitcnt lgkmcnt(3)
	v_pk_fma_f32 v[160:161], v[80:81], v[228:229], v[160:161] op_sel_hi:[1,0,1]
	s_nop 0
	v_pk_fma_f32 v[156:157], v[82:83], v[228:229], v[160:161] op_sel:[0,1,0]
	s_nop 0
	v_pk_fma_f32 v[156:157], v[86:87], v[230:231], v[156:157] op_sel_hi:[1,0,1]
	v_mov_b32_e32 v158, v231
	v_pk_fma_f32 v[160:161], v[90:91], v[158:159], v[156:157] op_sel_hi:[1,0,1]
	ds_read_b128 v[224:227], v182 offset:25600
	s_waitcnt lgkmcnt(3)
	v_pk_fma_f32 v[160:161], v[76:77], v[232:233], v[160:161] op_sel_hi:[1,0,1]
	s_nop 0
	v_pk_fma_f32 v[156:157], v[78:79], v[232:233], v[160:161] op_sel:[0,1,0]
	s_nop 0
	v_pk_fma_f32 v[156:157], v[84:85], v[234:235], v[156:157] op_sel_hi:[1,0,1]
	v_mov_b32_e32 v158, v235
	v_pk_fma_f32 v[160:161], v[88:89], v[158:159], v[156:157] op_sel_hi:[1,0,1]
	ds_read_b128 v[228:231], v182 offset:26624
	s_waitcnt lgkmcnt(3)
	v_pk_fma_f32 v[160:161], v[68:69], v[236:237], v[160:161] op_sel_hi:[1,0,1]
	s_nop 0
	v_pk_fma_f32 v[156:157], v[70:71], v[236:237], v[160:161] op_sel:[0,1,0]
	s_nop 0
	v_pk_fma_f32 v[156:157], v[72:73], v[238:239], v[156:157] op_sel_hi:[1,0,1]
	v_mov_b32_e32 v158, v239
	v_pk_fma_f32 v[156:157], v[74:75], v[158:159], v[156:157] op_sel_hi:[1,0,1]
	ds_read_b128 v[232:235], v182 offset:27648
	s_waitcnt lgkmcnt(3)
	v_pk_fma_f32 v[162:163], v[124:125], v[240:241], 0 op_sel_hi:[1,0,0]
	s_nop 0
	v_pk_fma_f32 v[158:159], v[126:127], v[240:241], v[162:163] op_sel:[0,1,0]
	s_nop 0
	v_pk_fma_f32 v[158:159], v[128:129], v[242:243], v[158:159] op_sel_hi:[1,0,1]
	v_mov_b32_e32 v160, v243
	v_pk_fma_f32 v[162:163], v[130:131], v[160:161], v[158:159] op_sel_hi:[1,0,1]
	ds_read_b128 v[236:239], v182 offset:28672
	s_waitcnt lgkmcnt(3)
	v_pk_fma_f32 v[162:163], v[112:113], v[224:225], v[162:163] op_sel_hi:[1,0,1]
	s_nop 0
	v_pk_fma_f32 v[158:159], v[114:115], v[224:225], v[162:163] op_sel:[0,1,0]
	s_nop 0
	v_pk_fma_f32 v[158:159], v[118:119], v[226:227], v[158:159] op_sel_hi:[1,0,1]
	v_mov_b32_e32 v160, v227
	v_pk_fma_f32 v[162:163], v[122:123], v[160:161], v[158:159] op_sel_hi:[1,0,1]
	ds_read_b128 v[240:243], v182 offset:29696
	s_waitcnt lgkmcnt(3)
	v_pk_fma_f32 v[162:163], v[108:109], v[228:229], v[162:163] op_sel_hi:[1,0,1]
	s_nop 0
	v_pk_fma_f32 v[158:159], v[110:111], v[228:229], v[162:163] op_sel:[0,1,0]
	s_nop 0
	v_pk_fma_f32 v[158:159], v[116:117], v[230:231], v[158:159] op_sel_hi:[1,0,1]
	v_mov_b32_e32 v160, v231
	v_pk_fma_f32 v[162:163], v[120:121], v[160:161], v[158:159] op_sel_hi:[1,0,1]
	ds_read_b128 v[224:227], v182 offset:30720
	s_waitcnt lgkmcnt(3)
; #define LAS __attribute__((address_space(3)))
; __device__ __forceinline__ void phase_norm2(const Params& p, const Ctx& F, const int l) {
;     ...
;         unsigned wro = (unsigned)(uintptr_t)wr; asm volatile("" : "+v"(wro));
;         const LAS float* wr2 = (const LAS float*)(uintptr_t)wro;
; #pragma unroll
;         for (int e = 0; e < 16; ++e) { f32x2 a = {0.f, 0.f};
; #pragma unroll
;             for (int j = 0; j < 8; ++j) { const f32x4 w = *((const LAS f32x4*)(wr2 + e * DM) + F.lane + 64 * j);
; #pragma unroll
;                 for (int c = 0; c < 4; ++c) a += vv[j][c] * w[c]; }
;             lg[e] = a; }
	v_pk_fma_f32 v[162:163], v[96:97], v[232:233], v[162:163] op_sel_hi:[1,0,1]
	s_nop 0
	v_pk_fma_f32 v[158:159], v[98:99], v[232:233], v[162:163] op_sel:[0,1,0]
	s_nop 0
	v_pk_fma_f32 v[158:159], v[102:103], v[234:235], v[158:159] op_sel_hi:[1,0,1]
	v_mov_b32_e32 v160, v235
	v_pk_fma_f32 v[162:163], v[106:107], v[160:161], v[158:159] op_sel_hi:[1,0,1]
	ds_read_b128 v[228:231], v182 offset:31744
	s_waitcnt lgkmcnt(3)
	v_pk_fma_f32 v[162:163], v[92:93], v[236:237], v[162:163] op_sel_hi:[1,0,1]
	s_nop 0
	v_pk_fma_f32 v[158:159], v[94:95], v[236:237], v[162:163] op_sel:[0,1,0]
	s_nop 0
	v_pk_fma_f32 v[158:159], v[100:101], v[238:239], v[158:159] op_sel_hi:[1,0,1]
	v_mov_b32_e32 v160, v239
	v_pk_fma_f32 v[162:163], v[104:105], v[160:161], v[158:159] op_sel_hi:[1,0,1]
	ds_read_b128 v[232:235], v182 offset:32768
	s_waitcnt lgkmcnt(3)
	v_pk_fma_f32 v[162:163], v[80:81], v[240:241], v[162:163] op_sel_hi:[1,0,1]
	s_nop 0
	v_pk_fma_f32 v[158:159], v[82:83], v[240:241], v[162:163] op_sel:[0,1,0]
	s_nop 0
	v_pk_fma_f32 v[158:159], v[86:87], v[242:243], v[158:159] op_sel_hi:[1,0,1]
	v_mov_b32_e32 v160, v243
	v_pk_fma_f32 v[162:163], v[90:91], v[160:161], v[158:159] op_sel_hi:[1,0,1]
	ds_read_b128 v[236:239], v182 offset:33792
	s_waitcnt lgkmcnt(3)
	v_pk_fma_f32 v[162:163], v[76:77], v[224:225], v[162:163] op_sel_hi:[1,0,1]
	s_nop 0
	v_pk_fma_f32 v[158:159], v[78:79], v[224:225], v[162:163] op_sel:[0,1,0]
	s_nop 0
	v_pk_fma_f32 v[158:159], v[84:85], v[226:227], v[158:159] op_sel_hi:[1,0,1]
	v_mov_b32_e32 v160, v227
	v_pk_fma_f32 v[162:163], v[88:89], v[160:161], v[158:159] op_sel_hi:[1,0,1]
	ds_read_b128 v[240:243], v182 offset:34816
	s_waitcnt lgkmcnt(3)
	v_pk_fma_f32 v[162:163], v[68:69], v[228:229], v[162:163] op_sel_hi:[1,0,1]
	s_nop 0
	v_pk_fma_f32 v[158:159], v[70:71], v[228:229], v[162:163] op_sel:[0,1,0]
	s_nop 0
	v_pk_fma_f32 v[158:159], v[72:73], v[230:231], v[158:159] op_sel_hi:[1,0,1]
	v_mov_b32_e32 v160, v231
	v_pk_fma_f32 v[158:159], v[74:75], v[160:161], v[158:159] op_sel_hi:[1,0,1]
	ds_read_b128 v[224:227], v182 offset:35840
	s_waitcnt lgkmcnt(3)
	v_pk_fma_f32 v[164:165], v[124:125], v[232:233], 0 op_sel_hi:[1,0,0]
	s_nop 0
	v_pk_fma_f32 v[160:161], v[126:127], v[232:233], v[164:165] op_sel:[0,1,0]
	s_nop 0
	v_pk_fma_f32 v[160:161], v[128:129], v[234:235], v[160:161] op_sel_hi:[1,0,1]
	v_mov_b32_e32 v162, v235
	v_pk_fma_f32 v[164:165], v[130:131], v[162:163], v[160:161] op_sel_hi:[1,0,1]
	ds_read_b128 v[228:231], v182 offset:36864
	s_waitcnt lgkmcnt(3)
	v_pk_fma_f32 v[164:165], v[112:113], v[236:237], v[164:165] op_sel_hi:[1,0,1]
	s_nop 0
	v_pk_fma_f32 v[160:161], v[114:115], v[236:237], v[164:165] op_sel:[0,1,0]
	s_nop 0
	v_pk_fma_f32 v[160:161], v[118:119], v[238:239], v[160:161] op_sel_hi:[1,0,1]
	v_mov_b32_e32 v162, v239
	v_pk_fma_f32 v[164:165], v[122:123], v[162:163], v[160:161] op_sel_hi:[1,0,1]
	ds_read_b128 v[232:235], v182 offset:37888
	s_waitcnt lgkmcnt(3)
	v_pk_fma_f32 v[164:165], v[108:109], v[240:241], v[164:165] op_sel_hi:[1,0,1]
	s_nop 0
	v_pk_fma_f32 v[160:161], v[110:111], v[240:241], v[164:165] op_sel:[0,1,0]
	s_nop 0
	v_pk_fma_f32 v[160:161], v[116:117], v[242:243], v[160:161] op_sel_hi:[1,0,1]
	v_mov_b32_e32 v162, v243
	v_pk_fma_f32 v[164:165], v[120:121], v[162:163], v[160:161] op_sel_hi:[1,0,1]
	ds_read_b128 v[236:239], v182 offset:38912
	s_waitcnt lgkmcnt(3)
	v_pk_fma_f32 v[164:165], v[96:97], v[224:225], v[164:165] op_sel_hi:[1,0,1]
	s_nop 0
	v_pk_fma_f32 v[160:161], v[98:99], v[224:225], v[164:165] op_sel:[0,1,0]
	s_nop 0
	v_pk_fma_f32 v[160:161], v[102:103], v[226:227], v[160:161] op_sel_hi:[1,0,1]
	v_mov_b32_e32 v162, v227
	v_pk_fma_f32 v[164:165], v[106:107], v[162:163], v[160:161] op_sel_hi:[1,0,1]
	ds_read_b128 v[240:243], v182 offset:39936
	s_waitcnt lgkmcnt(3)
	v_pk_fma_f32 v[164:165], v[92:93], v[228:229], v[164:165] op_sel_hi:[1,0,1]
	s_nop 0
	v_pk_fma_f32 v[160:161], v[94:95], v[228:229], v[164:165] op_sel:[0,1,0]
	s_nop 0
	v_pk_fma_f32 v[160:161], v[100:101], v[230:231], v[160:161] op_sel_hi:[1,0,1]
	v_mov_b32_e32 v162, v231
	v_pk_fma_f32 v[164:165], v[104:105], v[162:163], v[160:161] op_sel_hi:[1,0,1]
	ds_read_b128 v[224:227], v182 offset:40960
	s_waitcnt lgkmcnt(3)
	v_pk_fma_f32 v[164:165], v[80:81], v[232:233], v[164:165] op_sel_hi:[1,0,1]
	s_nop 0
	v_pk_fma_f32 v[160:161], v[82:83], v[232:233], v[164:165] op_sel:[0,1,0]
	s_nop 0
	v_pk_fma_f32 v[160:161], v[86:87], v[234:235], v[160:161] op_sel_hi:[1,0,1]
	v_mov_b32_e32 v162, v235
	v_pk_fma_f32 v[164:165], v[90:91], v[162:163], v[160:161] op_sel_hi:[1,0,1]
	ds_read_b128 v[228:231], v182 offset:41984
	s_waitcnt lgkmcnt(3)
	v_pk_fma_f32 v[164:165], v[76:77], v[236:237], v[164:165] op_sel_hi:[1,0,1]
	s_nop 0
	v_pk_fma_f32 v[160:161], v[78:79], v[236:237], v[164:165] op_sel:[0,1,0]
	s_nop 0
	v_pk_fma_f32 v[160:161], v[84:85], v[238:239], v[160:161] op_sel_hi:[1,0,1]
	v_mov_b32_e32 v162, v239
	v_pk_fma_f32 v[164:165], v[88:89], v[162:163], v[160:161] op_sel_hi:[1,0,1]
	ds_read_b128 v[232:235], v182 offset:43008
	s_waitcnt lgkmcnt(3)
	v_pk_fma_f32 v[164:165], v[68:69], v[240:241], v[164:165] op_sel_hi:[1,0,1]
	s_nop 0
	v_pk_fma_f32 v[160:161], v[70:71], v[240:241], v[164:165] op_sel:[0,1,0]
	s_nop 0
	v_pk_fma_f32 v[160:161], v[72:73], v[242:243], v[160:161] op_sel_hi:[1,0,1]
	v_mov_b32_e32 v162, v243
	v_pk_fma_f32 v[160:161], v[74:75], v[162:163], v[160:161] op_sel_hi:[1,0,1]
	ds_read_b128 v[236:239], v182 offset:44032
	s_waitcnt lgkmcnt(3)
	v_pk_fma_f32 v[166:167], v[124:125], v[224:225], 0 op_sel_hi:[1,0,0]
	s_nop 0
	v_pk_fma_f32 v[162:163], v[126:127], v[224:225], v[166:167] op_sel:[0,1,0]
	s_nop 0
	v_pk_fma_f32 v[162:163], v[128:129], v[226:227], v[162:163] op_sel_hi:[1,0,1]
	v_mov_b32_e32 v164, v227
	v_pk_fma_f32 v[166:167], v[130:131], v[164:165], v[162:163] op_sel_hi:[1,0,1]
	ds_read_b128 v[240:243], v182 offset:45056
	s_waitcnt lgkmcnt(3)
; #define LAS __attribute__((address_space(3)))
; __device__ __forceinline__ void phase_norm2(const Params& p, const Ctx& F, const int l) {
;     ...
;         unsigned wro = (unsigned)(uintptr_t)wr; asm volatile("" : "+v"(wro));
;         const LAS float* wr2 = (const LAS float*)(uintptr_t)wro;
; #pragma unroll
;         for (int e = 0; e < 16; ++e) { f32x2 a = {0.f, 0.f};
; #pragma unroll
;             for (int j = 0; j < 8; ++j) { const f32x4 w = *((const LAS f32x4*)(wr2 + e * DM) + F.lane + 64 * j);
; #pragma unroll
;                 for (int c = 0; c < 4; ++c) a += vv[j][c] * w[c]; }
;             lg[e] = a; }
	v_pk_fma_f32 v[166:167], v[112:113], v[228:229], v[166:167] op_sel_hi:[1,0,1]
	s_nop 0
	v_pk_fma_f32 v[162:163], v[114:115], v[228:229], v[166:167] op_sel:[0,1,0]
	s_nop 0
	v_pk_fma_f32 v[162:163], v[118:119], v[230:231], v[162:163] op_sel_hi:[1,0,1]
	v_mov_b32_e32 v164, v231
	v_pk_fma_f32 v[166:167], v[122:123], v[164:165], v[162:163] op_sel_hi:[1,0,1]
	ds_read_b128 v[224:227], v182 offset:46080
	s_waitcnt lgkmcnt(3)
	v_pk_fma_f32 v[166:167], v[108:109], v[232:233], v[166:167] op_sel_hi:[1,0,1]
	s_nop 0
	v_pk_fma_f32 v[162:163], v[110:111], v[232:233], v[166:167] op_sel:[0,1,0]
	s_nop 0
	v_pk_fma_f32 v[162:163], v[116:117], v[234:235], v[162:163] op_sel_hi:[1,0,1]
	v_mov_b32_e32 v164, v235
	v_pk_fma_f32 v[166:167], v[120:121], v[164:165], v[162:163] op_sel_hi:[1,0,1]
	ds_read_b128 v[228:231], v182 offset:47104
	s_waitcnt lgkmcnt(3)
	v_pk_fma_f32 v[166:167], v[96:97], v[236:237], v[166:167] op_sel_hi:[1,0,1]
	s_nop 0
	v_pk_fma_f32 v[162:163], v[98:99], v[236:237], v[166:167] op_sel:[0,1,0]
	s_nop 0
	v_pk_fma_f32 v[162:163], v[102:103], v[238:239], v[162:163] op_sel_hi:[1,0,1]
	v_mov_b32_e32 v164, v239
	v_pk_fma_f32 v[166:167], v[106:107], v[164:165], v[162:163] op_sel_hi:[1,0,1]
	ds_read_b128 v[232:235], v182 offset:48128
	s_waitcnt lgkmcnt(3)
	v_pk_fma_f32 v[166:167], v[92:93], v[240:241], v[166:167] op_sel_hi:[1,0,1]
	s_nop 0
	v_pk_fma_f32 v[162:163], v[94:95], v[240:241], v[166:167] op_sel:[0,1,0]
	s_nop 0
	v_pk_fma_f32 v[162:163], v[100:101], v[242:243], v[162:163] op_sel_hi:[1,0,1]
	v_mov_b32_e32 v164, v243
	v_pk_fma_f32 v[166:167], v[104:105], v[164:165], v[162:163] op_sel_hi:[1,0,1]
	ds_read_b128 v[236:239], v182 offset:49152
	s_waitcnt lgkmcnt(3)
	v_pk_fma_f32 v[166:167], v[80:81], v[224:225], v[166:167] op_sel_hi:[1,0,1]
	s_nop 0
	v_pk_fma_f32 v[162:163], v[82:83], v[224:225], v[166:167] op_sel:[0,1,0]
	s_nop 0
	v_pk_fma_f32 v[162:163], v[86:87], v[226:227], v[162:163] op_sel_hi:[1,0,1]
	v_mov_b32_e32 v164, v227
	v_pk_fma_f32 v[166:167], v[90:91], v[164:165], v[162:163] op_sel_hi:[1,0,1]
	ds_read_b128 v[240:243], v182 offset:50176
	s_waitcnt lgkmcnt(3)
	v_pk_fma_f32 v[166:167], v[76:77], v[228:229], v[166:167] op_sel_hi:[1,0,1]
	s_nop 0
	v_pk_fma_f32 v[162:163], v[78:79], v[228:229], v[166:167] op_sel:[0,1,0]
	s_nop 0
	v_pk_fma_f32 v[162:163], v[84:85], v[230:231], v[162:163] op_sel_hi:[1,0,1]
	v_mov_b32_e32 v164, v231
	v_pk_fma_f32 v[166:167], v[88:89], v[164:165], v[162:163] op_sel_hi:[1,0,1]
	ds_read_b128 v[224:227], v182 offset:51200
	s_waitcnt lgkmcnt(3)
	v_pk_fma_f32 v[166:167], v[68:69], v[232:233], v[166:167] op_sel_hi:[1,0,1]
	s_nop 0
	v_pk_fma_f32 v[162:163], v[70:71], v[232:233], v[166:167] op_sel:[0,1,0]
	s_nop 0
	v_pk_fma_f32 v[162:163], v[72:73], v[234:235], v[162:163] op_sel_hi:[1,0,1]
	v_mov_b32_e32 v164, v235
	v_pk_fma_f32 v[162:163], v[74:75], v[164:165], v[162:163] op_sel_hi:[1,0,1]
	ds_read_b128 v[228:231], v182 offset:52224
	s_waitcnt lgkmcnt(3)
	v_pk_fma_f32 v[168:169], v[124:125], v[236:237], 0 op_sel_hi:[1,0,0]
	s_nop 0
	v_pk_fma_f32 v[164:165], v[126:127], v[236:237], v[168:169] op_sel:[0,1,0]
	s_nop 0
	v_pk_fma_f32 v[164:165], v[128:129], v[238:239], v[164:165] op_sel_hi:[1,0,1]
	v_mov_b32_e32 v166, v239
	v_pk_fma_f32 v[168:169], v[130:131], v[166:167], v[164:165] op_sel_hi:[1,0,1]
	ds_read_b128 v[232:235], v182 offset:53248
	s_waitcnt lgkmcnt(3)
	v_pk_fma_f32 v[168:169], v[112:113], v[240:241], v[168:169] op_sel_hi:[1,0,1]
	s_nop 0
	v_pk_fma_f32 v[164:165], v[114:115], v[240:241], v[168:169] op_sel:[0,1,0]
	s_nop 0
	v_pk_fma_f32 v[164:165], v[118:119], v[242:243], v[164:165] op_sel_hi:[1,0,1]
	v_mov_b32_e32 v166, v243
	v_pk_fma_f32 v[168:169], v[122:123], v[166:167], v[164:165] op_sel_hi:[1,0,1]
	ds_read_b128 v[236:239], v182 offset:54272
	s_waitcnt lgkmcnt(3)
	v_pk_fma_f32 v[168:169], v[108:109], v[224:225], v[168:169] op_sel_hi:[1,0,1]
	s_nop 0
	v_pk_fma_f32 v[164:165], v[110:111], v[224:225], v[168:169] op_sel:[0,1,0]
	s_nop 0
	v_pk_fma_f32 v[164:165], v[116:117], v[226:227], v[164:165] op_sel_hi:[1,0,1]
	v_mov_b32_e32 v166, v227
	v_pk_fma_f32 v[168:169], v[120:121], v[166:167], v[164:165] op_sel_hi:[1,0,1]
	ds_read_b128 v[240:243], v182 offset:55296
	s_waitcnt lgkmcnt(3)
	v_pk_fma_f32 v[168:169], v[96:97], v[228:229], v[168:169] op_sel_hi:[1,0,1]
	s_nop 0
	v_pk_fma_f32 v[164:165], v[98:99], v[228:229], v[168:169] op_sel:[0,1,0]
	s_nop 0
	v_pk_fma_f32 v[164:165], v[102:103], v[230:231], v[164:165] op_sel_hi:[1,0,1]
	v_mov_b32_e32 v166, v231
	v_pk_fma_f32 v[168:169], v[106:107], v[166:167], v[164:165] op_sel_hi:[1,0,1]
	ds_read_b128 v[224:227], v182 offset:56320
	s_waitcnt lgkmcnt(3)
	v_pk_fma_f32 v[168:169], v[92:93], v[232:233], v[168:169] op_sel_hi:[1,0,1]
	s_nop 0
	v_pk_fma_f32 v[164:165], v[94:95], v[232:233], v[168:169] op_sel:[0,1,0]
	s_nop 0
	v_pk_fma_f32 v[164:165], v[100:101], v[234:235], v[164:165] op_sel_hi:[1,0,1]
	v_mov_b32_e32 v166, v235
	v_pk_fma_f32 v[168:169], v[104:105], v[166:167], v[164:165] op_sel_hi:[1,0,1]
	ds_read_b128 v[228:231], v182 offset:57344
	s_waitcnt lgkmcnt(3)
	v_pk_fma_f32 v[168:169], v[80:81], v[236:237], v[168:169] op_sel_hi:[1,0,1]
	s_nop 0
	v_pk_fma_f32 v[164:165], v[82:83], v[236:237], v[168:169] op_sel:[0,1,0]
	s_nop 0
	v_pk_fma_f32 v[164:165], v[86:87], v[238:239], v[164:165] op_sel_hi:[1,0,1]
	v_mov_b32_e32 v166, v239
	v_pk_fma_f32 v[168:169], v[90:91], v[166:167], v[164:165] op_sel_hi:[1,0,1]
	ds_read_b128 v[232:235], v182 offset:58368
	s_waitcnt lgkmcnt(3)
; #define LAS __attribute__((address_space(3)))
; __device__ __forceinline__ void phase_norm2(const Params& p, const Ctx& F, const int l) {
;     ...
;         unsigned wro = (unsigned)(uintptr_t)wr; asm volatile("" : "+v"(wro));
;         const LAS float* wr2 = (const LAS float*)(uintptr_t)wro;
; #pragma unroll
;         for (int e = 0; e < 16; ++e) { f32x2 a = {0.f, 0.f};
; #pragma unroll
;             for (int j = 0; j < 8; ++j) { const f32x4 w = *((const LAS f32x4*)(wr2 + e * DM) + F.lane + 64 * j);
; #pragma unroll
;                 for (int c = 0; c < 4; ++c) a += vv[j][c] * w[c]; }
;             lg[e] = a; }
	v_pk_fma_f32 v[168:169], v[76:77], v[240:241], v[168:169] op_sel_hi:[1,0,1]
	s_nop 0
	v_pk_fma_f32 v[164:165], v[78:79], v[240:241], v[168:169] op_sel:[0,1,0]
	s_nop 0
	v_pk_fma_f32 v[164:165], v[84:85], v[242:243], v[164:165] op_sel_hi:[1,0,1]
	v_mov_b32_e32 v166, v243
	v_pk_fma_f32 v[168:169], v[88:89], v[166:167], v[164:165] op_sel_hi:[1,0,1]
	ds_read_b128 v[236:239], v182 offset:59392
	s_waitcnt lgkmcnt(3)
	v_pk_fma_f32 v[168:169], v[68:69], v[224:225], v[168:169] op_sel_hi:[1,0,1]
	s_nop 0
	v_pk_fma_f32 v[164:165], v[70:71], v[224:225], v[168:169] op_sel:[0,1,0]
	s_nop 0
	v_pk_fma_f32 v[164:165], v[72:73], v[226:227], v[164:165] op_sel_hi:[1,0,1]
	v_mov_b32_e32 v166, v227
	v_pk_fma_f32 v[164:165], v[74:75], v[166:167], v[164:165] op_sel_hi:[1,0,1]
	ds_read_b128 v[240:243], v182 offset:60416
	s_waitcnt lgkmcnt(3)
	v_pk_fma_f32 v[170:171], v[124:125], v[228:229], 0 op_sel_hi:[1,0,0]
	s_nop 0
	v_pk_fma_f32 v[166:167], v[126:127], v[228:229], v[170:171] op_sel:[0,1,0]
	s_nop 0
	v_pk_fma_f32 v[166:167], v[128:129], v[230:231], v[166:167] op_sel_hi:[1,0,1]
	v_mov_b32_e32 v168, v231
	v_pk_fma_f32 v[170:171], v[130:131], v[168:169], v[166:167] op_sel_hi:[1,0,1]
	ds_read_b128 v[224:227], v182 offset:61440
	s_waitcnt lgkmcnt(3)
	v_pk_fma_f32 v[170:171], v[112:113], v[232:233], v[170:171] op_sel_hi:[1,0,1]
	s_nop 0
	v_pk_fma_f32 v[166:167], v[114:115], v[232:233], v[170:171] op_sel:[0,1,0]
	s_nop 0
	v_pk_fma_f32 v[166:167], v[118:119], v[234:235], v[166:167] op_sel_hi:[1,0,1]
	v_mov_b32_e32 v168, v235
	v_pk_fma_f32 v[170:171], v[122:123], v[168:169], v[166:167] op_sel_hi:[1,0,1]
	ds_read_b128 v[228:231], v182 offset:62464
	s_waitcnt lgkmcnt(3)
	v_pk_fma_f32 v[170:171], v[108:109], v[236:237], v[170:171] op_sel_hi:[1,0,1]
	s_nop 0
	v_pk_fma_f32 v[166:167], v[110:111], v[236:237], v[170:171] op_sel:[0,1,0]
	s_nop 0
	v_pk_fma_f32 v[166:167], v[116:117], v[238:239], v[166:167] op_sel_hi:[1,0,1]
	v_mov_b32_e32 v168, v239
	v_pk_fma_f32 v[170:171], v[120:121], v[168:169], v[166:167] op_sel_hi:[1,0,1]
	ds_read_b128 v[232:235], v182 offset:63488
	s_waitcnt lgkmcnt(3)
	v_pk_fma_f32 v[170:171], v[96:97], v[240:241], v[170:171] op_sel_hi:[1,0,1]
	s_nop 0
	v_pk_fma_f32 v[166:167], v[98:99], v[240:241], v[170:171] op_sel:[0,1,0]
	s_nop 0
	v_pk_fma_f32 v[166:167], v[102:103], v[242:243], v[166:167] op_sel_hi:[1,0,1]
	v_mov_b32_e32 v168, v243
	v_pk_fma_f32 v[170:171], v[106:107], v[168:169], v[166:167] op_sel_hi:[1,0,1]
	ds_read_b128 v[236:239], v182 offset:64512
	s_waitcnt lgkmcnt(3)
	v_pk_fma_f32 v[170:171], v[92:93], v[224:225], v[170:171] op_sel_hi:[1,0,1]
	s_nop 0
	v_pk_fma_f32 v[166:167], v[94:95], v[224:225], v[170:171] op_sel:[0,1,0]
	s_nop 0
	v_pk_fma_f32 v[166:167], v[100:101], v[226:227], v[166:167] op_sel_hi:[1,0,1]
	v_mov_b32_e32 v168, v227
	v_pk_fma_f32 v[170:171], v[104:105], v[168:169], v[166:167] op_sel_hi:[1,0,1]
	ds_read_b128 v[240:243], v244
	s_waitcnt lgkmcnt(3)
	v_pk_fma_f32 v[170:171], v[80:81], v[228:229], v[170:171] op_sel_hi:[1,0,1]
	s_nop 0
	v_pk_fma_f32 v[166:167], v[82:83], v[228:229], v[170:171] op_sel:[0,1,0]
	s_nop 0
	v_pk_fma_f32 v[166:167], v[86:87], v[230:231], v[166:167] op_sel_hi:[1,0,1]
	v_mov_b32_e32 v168, v231
	v_pk_fma_f32 v[170:171], v[90:91], v[168:169], v[166:167] op_sel_hi:[1,0,1]
	ds_read_b128 v[224:227], v244 offset:1024
	s_waitcnt lgkmcnt(3)
	v_pk_fma_f32 v[170:171], v[76:77], v[232:233], v[170:171] op_sel_hi:[1,0,1]
	s_nop 0
	v_pk_fma_f32 v[166:167], v[78:79], v[232:233], v[170:171] op_sel:[0,1,0]
	s_nop 0
	v_pk_fma_f32 v[166:167], v[84:85], v[234:235], v[166:167] op_sel_hi:[1,0,1]
	v_mov_b32_e32 v168, v235
	v_pk_fma_f32 v[170:171], v[88:89], v[168:169], v[166:167] op_sel_hi:[1,0,1]
	ds_read_b128 v[228:231], v244 offset:2048
	s_waitcnt lgkmcnt(3)
	v_pk_fma_f32 v[170:171], v[68:69], v[236:237], v[170:171] op_sel_hi:[1,0,1]
	s_nop 0
	v_pk_fma_f32 v[166:167], v[70:71], v[236:237], v[170:171] op_sel:[0,1,0]
	s_nop 0
	v_pk_fma_f32 v[166:167], v[72:73], v[238:239], v[166:167] op_sel_hi:[1,0,1]
	v_mov_b32_e32 v168, v239
	v_pk_fma_f32 v[166:167], v[74:75], v[168:169], v[166:167] op_sel_hi:[1,0,1]
	ds_read_b128 v[232:235], v244 offset:3072
	s_waitcnt lgkmcnt(3)
	v_pk_fma_f32 v[172:173], v[124:125], v[240:241], 0 op_sel_hi:[1,0,0]
	s_nop 0
	v_pk_fma_f32 v[168:169], v[126:127], v[240:241], v[172:173] op_sel:[0,1,0]
	s_nop 0
	v_pk_fma_f32 v[168:169], v[128:129], v[242:243], v[168:169] op_sel_hi:[1,0,1]
	v_mov_b32_e32 v170, v243
	v_pk_fma_f32 v[172:173], v[130:131], v[170:171], v[168:169] op_sel_hi:[1,0,1]
	ds_read_b128 v[236:239], v244 offset:4096
	s_waitcnt lgkmcnt(3)
	v_pk_fma_f32 v[172:173], v[112:113], v[224:225], v[172:173] op_sel_hi:[1,0,1]
	s_nop 0
	v_pk_fma_f32 v[168:169], v[114:115], v[224:225], v[172:173] op_sel:[0,1,0]
	s_nop 0
	v_pk_fma_f32 v[168:169], v[118:119], v[226:227], v[168:169] op_sel_hi:[1,0,1]
	v_mov_b32_e32 v170, v227
	v_pk_fma_f32 v[172:173], v[122:123], v[170:171], v[168:169] op_sel_hi:[1,0,1]
	ds_read_b128 v[240:243], v244 offset:5120
	s_waitcnt lgkmcnt(3)
	v_pk_fma_f32 v[172:173], v[108:109], v[228:229], v[172:173] op_sel_hi:[1,0,1]
	s_nop 0
	v_pk_fma_f32 v[168:169], v[110:111], v[228:229], v[172:173] op_sel:[0,1,0]
	s_nop 0
	v_pk_fma_f32 v[168:169], v[116:117], v[230:231], v[168:169] op_sel_hi:[1,0,1]
	v_mov_b32_e32 v170, v231
	v_pk_fma_f32 v[172:173], v[120:121], v[170:171], v[168:169] op_sel_hi:[1,0,1]
	ds_read_b128 v[224:227], v244 offset:6144
	s_waitcnt lgkmcnt(3)
	v_pk_fma_f32 v[172:173], v[96:97], v[232:233], v[172:173] op_sel_hi:[1,0,1]
	s_nop 0
	v_pk_fma_f32 v[168:169], v[98:99], v[232:233], v[172:173] op_sel:[0,1,0]
	s_nop 0
	v_pk_fma_f32 v[168:169], v[102:103], v[234:235], v[168:169] op_sel_hi:[1,0,1]
	v_mov_b32_e32 v170, v235
	v_pk_fma_f32 v[172:173], v[106:107], v[170:171], v[168:169] op_sel_hi:[1,0,1]
	ds_read_b128 v[228:231], v244 offset:7168
	s_waitcnt lgkmcnt(3)
; #define LAS __attribute__((address_space(3)))
; __device__ __forceinline__ void phase_norm2(const Params& p, const Ctx& F, const int l) {
;     ...
;         unsigned wro = (unsigned)(uintptr_t)wr; asm volatile("" : "+v"(wro));
;         const LAS float* wr2 = (const LAS float*)(uintptr_t)wro;
; #pragma unroll
;         for (int e = 0; e < 16; ++e) { f32x2 a = {0.f, 0.f};
; #pragma unroll
;             for (int j = 0; j < 8; ++j) { const f32x4 w = *((const LAS f32x4*)(wr2 + e * DM) + F.lane + 64 * j);
; #pragma unroll
;                 for (int c = 0; c < 4; ++c) a += vv[j][c] * w[c]; }
;             lg[e] = a; }
	v_pk_fma_f32 v[172:173], v[92:93], v[236:237], v[172:173] op_sel_hi:[1,0,1]
	s_nop 0
	v_pk_fma_f32 v[168:169], v[94:95], v[236:237], v[172:173] op_sel:[0,1,0]
	s_nop 0
	v_pk_fma_f32 v[168:169], v[100:101], v[238:239], v[168:169] op_sel_hi:[1,0,1]
	v_mov_b32_e32 v170, v239
	v_pk_fma_f32 v[172:173], v[104:105], v[170:171], v[168:169] op_sel_hi:[1,0,1]
	ds_read_b128 v[232:235], v244 offset:8192
	s_waitcnt lgkmcnt(3)
	v_pk_fma_f32 v[172:173], v[80:81], v[240:241], v[172:173] op_sel_hi:[1,0,1]
	s_nop 0
	v_pk_fma_f32 v[168:169], v[82:83], v[240:241], v[172:173] op_sel:[0,1,0]
	s_nop 0
	v_pk_fma_f32 v[168:169], v[86:87], v[242:243], v[168:169] op_sel_hi:[1,0,1]
	v_mov_b32_e32 v170, v243
	v_pk_fma_f32 v[172:173], v[90:91], v[170:171], v[168:169] op_sel_hi:[1,0,1]
	ds_read_b128 v[236:239], v244 offset:9216
	s_waitcnt lgkmcnt(3)
	v_pk_fma_f32 v[172:173], v[76:77], v[224:225], v[172:173] op_sel_hi:[1,0,1]
	s_nop 0
	v_pk_fma_f32 v[168:169], v[78:79], v[224:225], v[172:173] op_sel:[0,1,0]
	s_nop 0
	v_pk_fma_f32 v[168:169], v[84:85], v[226:227], v[168:169] op_sel_hi:[1,0,1]
	v_mov_b32_e32 v170, v227
	v_pk_fma_f32 v[172:173], v[88:89], v[170:171], v[168:169] op_sel_hi:[1,0,1]
	ds_read_b128 v[240:243], v244 offset:10240
	s_waitcnt lgkmcnt(3)
	v_pk_fma_f32 v[172:173], v[68:69], v[228:229], v[172:173] op_sel_hi:[1,0,1]
	s_nop 0
	v_pk_fma_f32 v[168:169], v[70:71], v[228:229], v[172:173] op_sel:[0,1,0]
	s_nop 0
	v_pk_fma_f32 v[168:169], v[72:73], v[230:231], v[168:169] op_sel_hi:[1,0,1]
	v_mov_b32_e32 v170, v231
	v_pk_fma_f32 v[168:169], v[74:75], v[170:171], v[168:169] op_sel_hi:[1,0,1]
	ds_read_b128 v[224:227], v244 offset:11264
	s_waitcnt lgkmcnt(3)
	v_pk_fma_f32 v[174:175], v[124:125], v[232:233], 0 op_sel_hi:[1,0,0]
	s_nop 0
	v_pk_fma_f32 v[170:171], v[126:127], v[232:233], v[174:175] op_sel:[0,1,0]
	s_nop 0
	v_pk_fma_f32 v[170:171], v[128:129], v[234:235], v[170:171] op_sel_hi:[1,0,1]
	v_mov_b32_e32 v172, v235
	v_pk_fma_f32 v[174:175], v[130:131], v[172:173], v[170:171] op_sel_hi:[1,0,1]
	ds_read_b128 v[228:231], v244 offset:12288
	s_waitcnt lgkmcnt(3)
	v_pk_fma_f32 v[174:175], v[112:113], v[236:237], v[174:175] op_sel_hi:[1,0,1]
	s_nop 0
	v_pk_fma_f32 v[170:171], v[114:115], v[236:237], v[174:175] op_sel:[0,1,0]
	s_nop 0
	v_pk_fma_f32 v[170:171], v[118:119], v[238:239], v[170:171] op_sel_hi:[1,0,1]
	v_mov_b32_e32 v172, v239
	v_pk_fma_f32 v[174:175], v[122:123], v[172:173], v[170:171] op_sel_hi:[1,0,1]
	ds_read_b128 v[232:235], v244 offset:13312
	s_waitcnt lgkmcnt(3)
	v_pk_fma_f32 v[174:175], v[108:109], v[240:241], v[174:175] op_sel_hi:[1,0,1]
	s_nop 0
	v_pk_fma_f32 v[170:171], v[110:111], v[240:241], v[174:175] op_sel:[0,1,0]
	s_nop 0
	v_pk_fma_f32 v[170:171], v[116:117], v[242:243], v[170:171] op_sel_hi:[1,0,1]
	v_mov_b32_e32 v172, v243
	v_pk_fma_f32 v[174:175], v[120:121], v[172:173], v[170:171] op_sel_hi:[1,0,1]
	ds_read_b128 v[236:239], v244 offset:14336
	s_waitcnt lgkmcnt(3)
	v_pk_fma_f32 v[174:175], v[96:97], v[224:225], v[174:175] op_sel_hi:[1,0,1]
	s_nop 0
	v_pk_fma_f32 v[170:171], v[98:99], v[224:225], v[174:175] op_sel:[0,1,0]
	s_nop 0
	v_pk_fma_f32 v[170:171], v[102:103], v[226:227], v[170:171] op_sel_hi:[1,0,1]
	v_mov_b32_e32 v172, v227
	v_pk_fma_f32 v[174:175], v[106:107], v[172:173], v[170:171] op_sel_hi:[1,0,1]
	ds_read_b128 v[240:243], v244 offset:15360
	s_waitcnt lgkmcnt(3)
	v_pk_fma_f32 v[174:175], v[92:93], v[228:229], v[174:175] op_sel_hi:[1,0,1]
	s_nop 0
	v_pk_fma_f32 v[170:171], v[94:95], v[228:229], v[174:175] op_sel:[0,1,0]
	s_nop 0
	v_pk_fma_f32 v[170:171], v[100:101], v[230:231], v[170:171] op_sel_hi:[1,0,1]
	v_mov_b32_e32 v172, v231
	v_pk_fma_f32 v[174:175], v[104:105], v[172:173], v[170:171] op_sel_hi:[1,0,1]
	ds_read_b128 v[224:227], v244 offset:16384
	s_waitcnt lgkmcnt(3)
	v_pk_fma_f32 v[174:175], v[80:81], v[232:233], v[174:175] op_sel_hi:[1,0,1]
	s_nop 0
	v_pk_fma_f32 v[170:171], v[82:83], v[232:233], v[174:175] op_sel:[0,1,0]
	s_nop 0
	v_pk_fma_f32 v[170:171], v[86:87], v[234:235], v[170:171] op_sel_hi:[1,0,1]
	v_mov_b32_e32 v172, v235
	v_pk_fma_f32 v[174:175], v[90:91], v[172:173], v[170:171] op_sel_hi:[1,0,1]
	ds_read_b128 v[228:231], v244 offset:17408
	s_waitcnt lgkmcnt(3)
	v_pk_fma_f32 v[174:175], v[76:77], v[236:237], v[174:175] op_sel_hi:[1,0,1]
	s_nop 0
	v_pk_fma_f32 v[170:171], v[78:79], v[236:237], v[174:175] op_sel:[0,1,0]
	s_nop 0
	v_pk_fma_f32 v[170:171], v[84:85], v[238:239], v[170:171] op_sel_hi:[1,0,1]
	v_mov_b32_e32 v172, v239
	v_pk_fma_f32 v[174:175], v[88:89], v[172:173], v[170:171] op_sel_hi:[1,0,1]
	ds_read_b128 v[232:235], v244 offset:18432
	s_waitcnt lgkmcnt(3)
	v_pk_fma_f32 v[174:175], v[68:69], v[240:241], v[174:175] op_sel_hi:[1,0,1]
	s_nop 0
	v_pk_fma_f32 v[170:171], v[70:71], v[240:241], v[174:175] op_sel:[0,1,0]
	s_nop 0
	v_pk_fma_f32 v[170:171], v[72:73], v[242:243], v[170:171] op_sel_hi:[1,0,1]
	v_mov_b32_e32 v172, v243
	v_pk_fma_f32 v[170:171], v[74:75], v[172:173], v[170:171] op_sel_hi:[1,0,1]
	ds_read_b128 v[236:239], v244 offset:19456
	s_waitcnt lgkmcnt(3)
	v_pk_fma_f32 v[176:177], v[124:125], v[224:225], 0 op_sel_hi:[1,0,0]
	s_nop 0
	v_pk_fma_f32 v[172:173], v[126:127], v[224:225], v[176:177] op_sel:[0,1,0]
	s_nop 0
	v_pk_fma_f32 v[172:173], v[128:129], v[226:227], v[172:173] op_sel_hi:[1,0,1]
	v_mov_b32_e32 v174, v227
	v_pk_fma_f32 v[176:177], v[130:131], v[174:175], v[172:173] op_sel_hi:[1,0,1]
	ds_read_b128 v[240:243], v244 offset:20480
	s_waitcnt lgkmcnt(3)
	v_pk_fma_f32 v[176:177], v[112:113], v[228:229], v[176:177] op_sel_hi:[1,0,1]
	s_nop 0
	v_pk_fma_f32 v[172:173], v[114:115], v[228:229], v[176:177] op_sel:[0,1,0]
	s_nop 0
	v_pk_fma_f32 v[172:173], v[118:119], v[230:231], v[172:173] op_sel_hi:[1,0,1]
	v_mov_b32_e32 v174, v231
	v_pk_fma_f32 v[176:177], v[122:123], v[174:175], v[172:173] op_sel_hi:[1,0,1]
	ds_read_b128 v[224:227], v244 offset:21504
	s_waitcnt lgkmcnt(3)
; #define LAS __attribute__((address_space(3)))
; __device__ __forceinline__ void phase_norm2(const Params& p, const Ctx& F, const int l) {
;     ...
;         unsigned wro = (unsigned)(uintptr_t)wr; asm volatile("" : "+v"(wro));
;         const LAS float* wr2 = (const LAS float*)(uintptr_t)wro;
; #pragma unroll
;         for (int e = 0; e < 16; ++e) { f32x2 a = {0.f, 0.f};
; #pragma unroll
;             for (int j = 0; j < 8; ++j) { const f32x4 w = *((const LAS f32x4*)(wr2 + e * DM) + F.lane + 64 * j);
; #pragma unroll
;                 for (int c = 0; c < 4; ++c) a += vv[j][c] * w[c]; }
;             lg[e] = a; }
	v_pk_fma_f32 v[176:177], v[108:109], v[232:233], v[176:177] op_sel_hi:[1,0,1]
	s_nop 0
	v_pk_fma_f32 v[172:173], v[110:111], v[232:233], v[176:177] op_sel:[0,1,0]
	s_nop 0
	v_pk_fma_f32 v[172:173], v[116:117], v[234:235], v[172:173] op_sel_hi:[1,0,1]
	v_mov_b32_e32 v174, v235
	v_pk_fma_f32 v[176:177], v[120:121], v[174:175], v[172:173] op_sel_hi:[1,0,1]
	ds_read_b128 v[228:231], v244 offset:22528
	s_waitcnt lgkmcnt(3)
	v_pk_fma_f32 v[176:177], v[96:97], v[236:237], v[176:177] op_sel_hi:[1,0,1]
	s_nop 0
	v_pk_fma_f32 v[172:173], v[98:99], v[236:237], v[176:177] op_sel:[0,1,0]
	s_nop 0
	v_pk_fma_f32 v[172:173], v[102:103], v[238:239], v[172:173] op_sel_hi:[1,0,1]
	v_mov_b32_e32 v174, v239
	v_pk_fma_f32 v[176:177], v[106:107], v[174:175], v[172:173] op_sel_hi:[1,0,1]
	ds_read_b128 v[232:235], v244 offset:23552
	s_waitcnt lgkmcnt(3)
	v_pk_fma_f32 v[176:177], v[92:93], v[240:241], v[176:177] op_sel_hi:[1,0,1]
	s_nop 0
	v_pk_fma_f32 v[172:173], v[94:95], v[240:241], v[176:177] op_sel:[0,1,0]
	s_nop 0
	v_pk_fma_f32 v[172:173], v[100:101], v[242:243], v[172:173] op_sel_hi:[1,0,1]
	v_mov_b32_e32 v174, v243
	v_pk_fma_f32 v[176:177], v[104:105], v[174:175], v[172:173] op_sel_hi:[1,0,1]
	ds_read_b128 v[236:239], v244 offset:24576
	s_waitcnt lgkmcnt(3)
	v_pk_fma_f32 v[176:177], v[80:81], v[224:225], v[176:177] op_sel_hi:[1,0,1]
	s_nop 0
	v_pk_fma_f32 v[172:173], v[82:83], v[224:225], v[176:177] op_sel:[0,1,0]
	s_nop 0
	v_pk_fma_f32 v[172:173], v[86:87], v[226:227], v[172:173] op_sel_hi:[1,0,1]
	v_mov_b32_e32 v174, v227
	v_pk_fma_f32 v[176:177], v[90:91], v[174:175], v[172:173] op_sel_hi:[1,0,1]
	ds_read_b128 v[240:243], v244 offset:25600
	s_waitcnt lgkmcnt(3)
	v_pk_fma_f32 v[176:177], v[76:77], v[228:229], v[176:177] op_sel_hi:[1,0,1]
	s_nop 0
	v_pk_fma_f32 v[172:173], v[78:79], v[228:229], v[176:177] op_sel:[0,1,0]
	s_nop 0
	v_pk_fma_f32 v[172:173], v[84:85], v[230:231], v[172:173] op_sel_hi:[1,0,1]
	v_mov_b32_e32 v174, v231
	v_pk_fma_f32 v[176:177], v[88:89], v[174:175], v[172:173] op_sel_hi:[1,0,1]
	ds_read_b128 v[224:227], v244 offset:26624
	s_waitcnt lgkmcnt(3)
	v_pk_fma_f32 v[176:177], v[68:69], v[232:233], v[176:177] op_sel_hi:[1,0,1]
	s_nop 0
	v_pk_fma_f32 v[172:173], v[70:71], v[232:233], v[176:177] op_sel:[0,1,0]
	s_nop 0
	v_pk_fma_f32 v[172:173], v[72:73], v[234:235], v[172:173] op_sel_hi:[1,0,1]
	v_mov_b32_e32 v174, v235
	v_pk_fma_f32 v[172:173], v[74:75], v[174:175], v[172:173] op_sel_hi:[1,0,1]
	ds_read_b128 v[228:231], v244 offset:27648
	s_waitcnt lgkmcnt(3)
	v_pk_fma_f32 v[178:179], v[124:125], v[236:237], 0 op_sel_hi:[1,0,0]
	s_nop 0
	v_pk_fma_f32 v[174:175], v[126:127], v[236:237], v[178:179] op_sel:[0,1,0]
	s_nop 0
	v_pk_fma_f32 v[174:175], v[128:129], v[238:239], v[174:175] op_sel_hi:[1,0,1]
	v_mov_b32_e32 v176, v239
	v_pk_fma_f32 v[178:179], v[130:131], v[176:177], v[174:175] op_sel_hi:[1,0,1]
	ds_read_b128 v[232:235], v244 offset:28672
	s_waitcnt lgkmcnt(3)
	v_pk_fma_f32 v[178:179], v[112:113], v[240:241], v[178:179] op_sel_hi:[1,0,1]
	s_nop 0
	v_pk_fma_f32 v[174:175], v[114:115], v[240:241], v[178:179] op_sel:[0,1,0]
	s_nop 0
	v_pk_fma_f32 v[174:175], v[118:119], v[242:243], v[174:175] op_sel_hi:[1,0,1]
	v_mov_b32_e32 v176, v243
	v_pk_fma_f32 v[178:179], v[122:123], v[176:177], v[174:175] op_sel_hi:[1,0,1]
	ds_read_b128 v[236:239], v244 offset:29696
	s_waitcnt lgkmcnt(3)
	v_pk_fma_f32 v[178:179], v[108:109], v[224:225], v[178:179] op_sel_hi:[1,0,1]
	s_nop 0
	v_pk_fma_f32 v[174:175], v[110:111], v[224:225], v[178:179] op_sel:[0,1,0]
	s_nop 0
	v_pk_fma_f32 v[174:175], v[116:117], v[226:227], v[174:175] op_sel_hi:[1,0,1]
	v_mov_b32_e32 v176, v227
	v_pk_fma_f32 v[178:179], v[120:121], v[176:177], v[174:175] op_sel_hi:[1,0,1]
	ds_read_b128 v[240:243], v244 offset:30720
	s_waitcnt lgkmcnt(3)
	v_pk_fma_f32 v[178:179], v[96:97], v[228:229], v[178:179] op_sel_hi:[1,0,1]
	s_nop 0
	v_pk_fma_f32 v[174:175], v[98:99], v[228:229], v[178:179] op_sel:[0,1,0]
	s_nop 0
	v_pk_fma_f32 v[174:175], v[102:103], v[230:231], v[174:175] op_sel_hi:[1,0,1]
	v_mov_b32_e32 v176, v231
	v_pk_fma_f32 v[178:179], v[106:107], v[176:177], v[174:175] op_sel_hi:[1,0,1]
	ds_read_b128 v[224:227], v244 offset:31744
	s_waitcnt lgkmcnt(3)
	v_pk_fma_f32 v[178:179], v[92:93], v[232:233], v[178:179] op_sel_hi:[1,0,1]
	s_nop 0
	v_pk_fma_f32 v[174:175], v[94:95], v[232:233], v[178:179] op_sel:[0,1,0]
	s_nop 0
	v_pk_fma_f32 v[174:175], v[100:101], v[234:235], v[174:175] op_sel_hi:[1,0,1]
	v_mov_b32_e32 v176, v235
	v_pk_fma_f32 v[178:179], v[104:105], v[176:177], v[174:175] op_sel_hi:[1,0,1]
	ds_read_b128 v[228:231], v244 offset:32768
	s_waitcnt lgkmcnt(3)
	v_pk_fma_f32 v[178:179], v[80:81], v[236:237], v[178:179] op_sel_hi:[1,0,1]
	s_nop 0
	v_pk_fma_f32 v[174:175], v[82:83], v[236:237], v[178:179] op_sel:[0,1,0]
	s_nop 0
	v_pk_fma_f32 v[174:175], v[86:87], v[238:239], v[174:175] op_sel_hi:[1,0,1]
	v_mov_b32_e32 v176, v239
	v_pk_fma_f32 v[178:179], v[90:91], v[176:177], v[174:175] op_sel_hi:[1,0,1]
	ds_read_b128 v[232:235], v244 offset:33792
	s_waitcnt lgkmcnt(3)
	v_pk_fma_f32 v[178:179], v[76:77], v[240:241], v[178:179] op_sel_hi:[1,0,1]
	s_nop 0
	v_pk_fma_f32 v[174:175], v[78:79], v[240:241], v[178:179] op_sel:[0,1,0]
	s_nop 0
	v_pk_fma_f32 v[174:175], v[84:85], v[242:243], v[174:175] op_sel_hi:[1,0,1]
	v_mov_b32_e32 v176, v243
	v_pk_fma_f32 v[178:179], v[88:89], v[176:177], v[174:175] op_sel_hi:[1,0,1]
	ds_read_b128 v[236:239], v244 offset:34816
	s_waitcnt lgkmcnt(3)
; #define LAS __attribute__((address_space(3)))
; __device__ __forceinline__ void phase_norm2(const Params& p, const Ctx& F, const int l) {
;     ...
;         unsigned wro = (unsigned)(uintptr_t)wr; asm volatile("" : "+v"(wro));
;         const LAS float* wr2 = (const LAS float*)(uintptr_t)wro;
; #pragma unroll
;         for (int e = 0; e < 16; ++e) { f32x2 a = {0.f, 0.f};
; #pragma unroll
;             for (int j = 0; j < 8; ++j) { const f32x4 w = *((const LAS f32x4*)(wr2 + e * DM) + F.lane + 64 * j);
; #pragma unroll
;                 for (int c = 0; c < 4; ++c) a += vv[j][c] * w[c]; }
;             lg[e] = a; }
	v_pk_fma_f32 v[178:179], v[68:69], v[224:225], v[178:179] op_sel_hi:[1,0,1]
	s_nop 0
	v_pk_fma_f32 v[174:175], v[70:71], v[224:225], v[178:179] op_sel:[0,1,0]
	s_nop 0
	v_pk_fma_f32 v[174:175], v[72:73], v[226:227], v[174:175] op_sel_hi:[1,0,1]
	v_mov_b32_e32 v176, v227
	v_pk_fma_f32 v[174:175], v[74:75], v[176:177], v[174:175] op_sel_hi:[1,0,1]
	ds_read_b128 v[240:243], v244 offset:35840
	s_waitcnt lgkmcnt(3)
	v_pk_fma_f32 v[180:181], v[124:125], v[228:229], 0 op_sel_hi:[1,0,0]
	s_nop 0
	v_pk_fma_f32 v[176:177], v[126:127], v[228:229], v[180:181] op_sel:[0,1,0]
	s_nop 0
	v_pk_fma_f32 v[176:177], v[128:129], v[230:231], v[176:177] op_sel_hi:[1,0,1]
	v_mov_b32_e32 v178, v231
	v_pk_fma_f32 v[180:181], v[130:131], v[178:179], v[176:177] op_sel_hi:[1,0,1]
	ds_read_b128 v[224:227], v244 offset:36864
	s_waitcnt lgkmcnt(3)
	v_pk_fma_f32 v[180:181], v[112:113], v[232:233], v[180:181] op_sel_hi:[1,0,1]
	s_nop 0
	v_pk_fma_f32 v[176:177], v[114:115], v[232:233], v[180:181] op_sel:[0,1,0]
	s_nop 0
	v_pk_fma_f32 v[176:177], v[118:119], v[234:235], v[176:177] op_sel_hi:[1,0,1]
	v_mov_b32_e32 v178, v235
	v_pk_fma_f32 v[180:181], v[122:123], v[178:179], v[176:177] op_sel_hi:[1,0,1]
	ds_read_b128 v[228:231], v244 offset:37888
	s_waitcnt lgkmcnt(3)
	v_pk_fma_f32 v[180:181], v[108:109], v[236:237], v[180:181] op_sel_hi:[1,0,1]
	s_nop 0
	v_pk_fma_f32 v[176:177], v[110:111], v[236:237], v[180:181] op_sel:[0,1,0]
	s_nop 0
	v_pk_fma_f32 v[176:177], v[116:117], v[238:239], v[176:177] op_sel_hi:[1,0,1]
	v_mov_b32_e32 v178, v239
	v_pk_fma_f32 v[180:181], v[120:121], v[178:179], v[176:177] op_sel_hi:[1,0,1]
	ds_read_b128 v[232:235], v244 offset:38912
	s_waitcnt lgkmcnt(3)
	v_pk_fma_f32 v[180:181], v[96:97], v[240:241], v[180:181] op_sel_hi:[1,0,1]
	s_nop 0
	v_pk_fma_f32 v[176:177], v[98:99], v[240:241], v[180:181] op_sel:[0,1,0]
	s_nop 0
	v_pk_fma_f32 v[176:177], v[102:103], v[242:243], v[176:177] op_sel_hi:[1,0,1]
	v_mov_b32_e32 v178, v243
	v_pk_fma_f32 v[180:181], v[106:107], v[178:179], v[176:177] op_sel_hi:[1,0,1]
	ds_read_b128 v[236:239], v244 offset:39936
	s_waitcnt lgkmcnt(3)
	v_pk_fma_f32 v[180:181], v[92:93], v[224:225], v[180:181] op_sel_hi:[1,0,1]
	s_nop 0
	v_pk_fma_f32 v[176:177], v[94:95], v[224:225], v[180:181] op_sel:[0,1,0]
	s_nop 0
	v_pk_fma_f32 v[176:177], v[100:101], v[226:227], v[176:177] op_sel_hi:[1,0,1]
	v_mov_b32_e32 v178, v227
	v_pk_fma_f32 v[180:181], v[104:105], v[178:179], v[176:177] op_sel_hi:[1,0,1]
	ds_read_b128 v[240:243], v244 offset:40960
	s_waitcnt lgkmcnt(3)
	v_pk_fma_f32 v[180:181], v[80:81], v[228:229], v[180:181] op_sel_hi:[1,0,1]
	s_nop 0
	v_pk_fma_f32 v[176:177], v[82:83], v[228:229], v[180:181] op_sel:[0,1,0]
	s_nop 0
	v_pk_fma_f32 v[176:177], v[86:87], v[230:231], v[176:177] op_sel_hi:[1,0,1]
	v_mov_b32_e32 v178, v231
	v_pk_fma_f32 v[180:181], v[90:91], v[178:179], v[176:177] op_sel_hi:[1,0,1]
	ds_read_b128 v[224:227], v244 offset:41984
	s_waitcnt lgkmcnt(3)
	v_pk_fma_f32 v[180:181], v[76:77], v[232:233], v[180:181] op_sel_hi:[1,0,1]
	s_nop 0
	v_pk_fma_f32 v[176:177], v[78:79], v[232:233], v[180:181] op_sel:[0,1,0]
	s_nop 0
	v_pk_fma_f32 v[176:177], v[84:85], v[234:235], v[176:177] op_sel_hi:[1,0,1]
	v_mov_b32_e32 v178, v235
	v_pk_fma_f32 v[180:181], v[88:89], v[178:179], v[176:177] op_sel_hi:[1,0,1]
	ds_read_b128 v[228:231], v244 offset:43008
	s_waitcnt lgkmcnt(3)
	v_pk_fma_f32 v[180:181], v[68:69], v[236:237], v[180:181] op_sel_hi:[1,0,1]
	s_nop 0
	v_pk_fma_f32 v[176:177], v[70:71], v[236:237], v[180:181] op_sel:[0,1,0]
	s_nop 0
	v_pk_fma_f32 v[176:177], v[72:73], v[238:239], v[176:177] op_sel_hi:[1,0,1]
	v_mov_b32_e32 v178, v239
	v_pk_fma_f32 v[176:177], v[74:75], v[178:179], v[176:177] op_sel_hi:[1,0,1]
	ds_read_b128 v[232:235], v244 offset:44032
	s_waitcnt lgkmcnt(3)
	v_pk_fma_f32 v[184:185], v[124:125], v[240:241], 0 op_sel_hi:[1,0,0]
	s_nop 0
	v_pk_fma_f32 v[178:179], v[126:127], v[240:241], v[184:185] op_sel:[0,1,0]
	s_nop 0
	v_pk_fma_f32 v[178:179], v[128:129], v[242:243], v[178:179] op_sel_hi:[1,0,1]
	v_mov_b32_e32 v180, v243
	v_pk_fma_f32 v[184:185], v[130:131], v[180:181], v[178:179] op_sel_hi:[1,0,1]
	ds_read_b128 v[236:239], v244 offset:45056
	s_waitcnt lgkmcnt(3)
	v_pk_fma_f32 v[184:185], v[112:113], v[224:225], v[184:185] op_sel_hi:[1,0,1]
	s_nop 0
	v_pk_fma_f32 v[178:179], v[114:115], v[224:225], v[184:185] op_sel:[0,1,0]
	s_nop 0
	v_pk_fma_f32 v[178:179], v[118:119], v[226:227], v[178:179] op_sel_hi:[1,0,1]
	v_mov_b32_e32 v180, v227
	v_pk_fma_f32 v[184:185], v[122:123], v[180:181], v[178:179] op_sel_hi:[1,0,1]
	ds_read_b128 v[240:243], v244 offset:46080
	s_waitcnt lgkmcnt(3)
	v_pk_fma_f32 v[184:185], v[108:109], v[228:229], v[184:185] op_sel_hi:[1,0,1]
	s_nop 0
	v_pk_fma_f32 v[178:179], v[110:111], v[228:229], v[184:185] op_sel:[0,1,0]
	s_nop 0
	v_pk_fma_f32 v[178:179], v[116:117], v[230:231], v[178:179] op_sel_hi:[1,0,1]
	v_mov_b32_e32 v180, v231
	v_pk_fma_f32 v[184:185], v[120:121], v[180:181], v[178:179] op_sel_hi:[1,0,1]
	ds_read_b128 v[224:227], v244 offset:47104
	s_waitcnt lgkmcnt(3)
	v_pk_fma_f32 v[184:185], v[96:97], v[232:233], v[184:185] op_sel_hi:[1,0,1]
	s_nop 0
	v_pk_fma_f32 v[178:179], v[98:99], v[232:233], v[184:185] op_sel:[0,1,0]
	s_nop 0
	v_pk_fma_f32 v[178:179], v[102:103], v[234:235], v[178:179] op_sel_hi:[1,0,1]
	v_mov_b32_e32 v180, v235
	v_pk_fma_f32 v[184:185], v[106:107], v[180:181], v[178:179] op_sel_hi:[1,0,1]
	ds_read_b128 v[228:231], v244 offset:48128
	s_waitcnt lgkmcnt(3)
; #define LAS __attribute__((address_space(3)))
; __device__ __forceinline__ void phase_norm2(const Params& p, const Ctx& F, const int l) {
;     ...
;         unsigned wro = (unsigned)(uintptr_t)wr; asm volatile("" : "+v"(wro));
;         const LAS float* wr2 = (const LAS float*)(uintptr_t)wro;
; #pragma unroll
;         for (int e = 0; e < 16; ++e) { f32x2 a = {0.f, 0.f};
; #pragma unroll
;             for (int j = 0; j < 8; ++j) { const f32x4 w = *((const LAS f32x4*)(wr2 + e * DM) + F.lane + 64 * j);
; #pragma unroll
;                 for (int c = 0; c < 4; ++c) a += vv[j][c] * w[c]; }
;             lg[e] = a; }
	v_pk_fma_f32 v[184:185], v[92:93], v[236:237], v[184:185] op_sel_hi:[1,0,1]
	s_nop 0
	v_pk_fma_f32 v[178:179], v[94:95], v[236:237], v[184:185] op_sel:[0,1,0]
	s_nop 0
	v_pk_fma_f32 v[178:179], v[100:101], v[238:239], v[178:179] op_sel_hi:[1,0,1]
	v_mov_b32_e32 v180, v239
	v_pk_fma_f32 v[184:185], v[104:105], v[180:181], v[178:179] op_sel_hi:[1,0,1]
	ds_read_b128 v[232:235], v244 offset:49152
	s_waitcnt lgkmcnt(3)
	v_pk_fma_f32 v[184:185], v[80:81], v[240:241], v[184:185] op_sel_hi:[1,0,1]
	s_nop 0
	v_pk_fma_f32 v[178:179], v[82:83], v[240:241], v[184:185] op_sel:[0,1,0]
	s_nop 0
	v_pk_fma_f32 v[178:179], v[86:87], v[242:243], v[178:179] op_sel_hi:[1,0,1]
	v_mov_b32_e32 v180, v243
	v_pk_fma_f32 v[184:185], v[90:91], v[180:181], v[178:179] op_sel_hi:[1,0,1]
	ds_read_b128 v[236:239], v244 offset:50176
	s_waitcnt lgkmcnt(3)
	v_pk_fma_f32 v[184:185], v[76:77], v[224:225], v[184:185] op_sel_hi:[1,0,1]
	s_nop 0
	v_pk_fma_f32 v[178:179], v[78:79], v[224:225], v[184:185] op_sel:[0,1,0]
	s_nop 0
	v_pk_fma_f32 v[178:179], v[84:85], v[226:227], v[178:179] op_sel_hi:[1,0,1]
	v_mov_b32_e32 v180, v227
	v_pk_fma_f32 v[184:185], v[88:89], v[180:181], v[178:179] op_sel_hi:[1,0,1]
	ds_read_b128 v[240:243], v244 offset:51200
	s_waitcnt lgkmcnt(3)
	v_pk_fma_f32 v[184:185], v[68:69], v[228:229], v[184:185] op_sel_hi:[1,0,1]
	s_nop 0
	v_pk_fma_f32 v[178:179], v[70:71], v[228:229], v[184:185] op_sel:[0,1,0]
	ds_read_b128 v[224:227], v244 offset:52224
	v_pk_fma_f32 v[178:179], v[72:73], v[230:231], v[178:179] op_sel_hi:[1,0,1]
	v_mov_b32_e32 v180, v231
	v_pk_fma_f32 v[178:179], v[74:75], v[180:181], v[178:179] op_sel_hi:[1,0,1]
	s_waitcnt lgkmcnt(3)
	v_pk_fma_f32 v[180:181], v[124:125], v[232:233], 0 op_sel_hi:[1,0,0]
	s_nop 0
	v_pk_fma_f32 v[180:181], v[126:127], v[232:233], v[180:181] op_sel:[0,1,0]
	v_mov_b32_e32 v184, v235
	v_pk_fma_f32 v[180:181], v[128:129], v[234:235], v[180:181] op_sel_hi:[1,0,1]
	s_nop 0
	v_pk_fma_f32 v[180:181], v[130:131], v[184:185], v[180:181] op_sel_hi:[1,0,1]
	ds_read_b128 v[228:231], v244 offset:53248
	s_waitcnt lgkmcnt(3)
	v_pk_fma_f32 v[180:181], v[112:113], v[236:237], v[180:181] op_sel_hi:[1,0,1]
	s_nop 0
	v_pk_fma_f32 v[180:181], v[114:115], v[236:237], v[180:181] op_sel:[0,1,0]
	v_mov_b32_e32 v184, v239
	v_pk_fma_f32 v[180:181], v[118:119], v[238:239], v[180:181] op_sel_hi:[1,0,1]
	s_nop 0
	v_pk_fma_f32 v[180:181], v[122:123], v[184:185], v[180:181] op_sel_hi:[1,0,1]
	ds_read_b128 v[232:235], v244 offset:54272
	s_waitcnt lgkmcnt(3)
	v_pk_fma_f32 v[180:181], v[108:109], v[240:241], v[180:181] op_sel_hi:[1,0,1]
	s_nop 0
	v_pk_fma_f32 v[180:181], v[110:111], v[240:241], v[180:181] op_sel:[0,1,0]
	v_mov_b32_e32 v184, v243
	v_pk_fma_f32 v[180:181], v[116:117], v[242:243], v[180:181] op_sel_hi:[1,0,1]
	s_nop 0
	v_pk_fma_f32 v[180:181], v[120:121], v[184:185], v[180:181] op_sel_hi:[1,0,1]
	ds_read_b128 v[236:239], v244 offset:55296
	s_waitcnt lgkmcnt(3)
	v_pk_fma_f32 v[180:181], v[96:97], v[224:225], v[180:181] op_sel_hi:[1,0,1]
	s_nop 0
	v_pk_fma_f32 v[180:181], v[98:99], v[224:225], v[180:181] op_sel:[0,1,0]
	v_mov_b32_e32 v184, v227
	v_pk_fma_f32 v[180:181], v[102:103], v[226:227], v[180:181] op_sel_hi:[1,0,1]
	s_nop 0
	v_pk_fma_f32 v[180:181], v[106:107], v[184:185], v[180:181] op_sel_hi:[1,0,1]
	ds_read_b128 v[240:243], v244 offset:56320
	s_waitcnt lgkmcnt(3)
	v_pk_fma_f32 v[180:181], v[92:93], v[228:229], v[180:181] op_sel_hi:[1,0,1]
	s_nop 0
	v_pk_fma_f32 v[180:181], v[94:95], v[228:229], v[180:181] op_sel:[0,1,0]
	v_mov_b32_e32 v184, v231
	v_pk_fma_f32 v[180:181], v[100:101], v[230:231], v[180:181] op_sel_hi:[1,0,1]
	s_nop 0
	v_pk_fma_f32 v[180:181], v[104:105], v[184:185], v[180:181] op_sel_hi:[1,0,1]
	ds_read_b128 v[224:227], v244 offset:57344
	s_waitcnt lgkmcnt(3)
	v_pk_fma_f32 v[180:181], v[80:81], v[232:233], v[180:181] op_sel_hi:[1,0,1]
	s_nop 0
	v_pk_fma_f32 v[180:181], v[82:83], v[232:233], v[180:181] op_sel:[0,1,0]
	v_mov_b32_e32 v184, v235
	v_pk_fma_f32 v[180:181], v[86:87], v[234:235], v[180:181] op_sel_hi:[1,0,1]
	s_nop 0
	v_pk_fma_f32 v[180:181], v[90:91], v[184:185], v[180:181] op_sel_hi:[1,0,1]
	ds_read_b128 v[228:231], v244 offset:58368
	s_waitcnt lgkmcnt(3)
	v_pk_fma_f32 v[180:181], v[76:77], v[236:237], v[180:181] op_sel_hi:[1,0,1]
	s_nop 0
	v_pk_fma_f32 v[180:181], v[78:79], v[236:237], v[180:181] op_sel:[0,1,0]
	v_mov_b32_e32 v184, v239
	v_pk_fma_f32 v[180:181], v[84:85], v[238:239], v[180:181] op_sel_hi:[1,0,1]
	s_nop 0
	v_pk_fma_f32 v[180:181], v[88:89], v[184:185], v[180:181] op_sel_hi:[1,0,1]
	ds_read_b128 v[232:235], v244 offset:59392
	s_waitcnt lgkmcnt(3)
	v_pk_fma_f32 v[180:181], v[68:69], v[240:241], v[180:181] op_sel_hi:[1,0,1]
	s_nop 0
	v_pk_fma_f32 v[180:181], v[70:71], v[240:241], v[180:181] op_sel:[0,1,0]
	v_mov_b32_e32 v184, v243
	v_pk_fma_f32 v[180:181], v[72:73], v[242:243], v[180:181] op_sel_hi:[1,0,1]
	s_nop 0
	v_pk_fma_f32 v[180:181], v[74:75], v[184:185], v[180:181] op_sel_hi:[1,0,1]
	ds_read_b128 v[236:239], v244 offset:60416
	s_waitcnt lgkmcnt(3)
	v_pk_fma_f32 v[124:125], v[124:125], v[224:225], 0 op_sel_hi:[1,0,0]
	s_nop 0
	v_pk_fma_f32 v[124:125], v[126:127], v[224:225], v[124:125] op_sel:[0,1,0]
	v_mov_b32_e32 v126, v227
	v_pk_fma_f32 v[124:125], v[128:129], v[226:227], v[124:125] op_sel_hi:[1,0,1]
	s_nop 0
	v_pk_fma_f32 v[128:129], v[130:131], v[126:127], v[124:125] op_sel_hi:[1,0,1]
	ds_read_b128 v[240:243], v244 offset:61440
	s_waitcnt lgkmcnt(3)
	v_pk_fma_f32 v[112:113], v[112:113], v[228:229], v[128:129] op_sel_hi:[1,0,1]
	s_nop 0
	v_pk_fma_f32 v[112:113], v[114:115], v[228:229], v[112:113] op_sel:[0,1,0]
	v_mov_b32_e32 v114, v231
	v_pk_fma_f32 v[112:113], v[118:119], v[230:231], v[112:113] op_sel_hi:[1,0,1]
	s_nop 0
	v_pk_fma_f32 v[118:119], v[122:123], v[114:115], v[112:113] op_sel_hi:[1,0,1]
	ds_read_b128 v[224:227], v244 offset:62464
	s_waitcnt lgkmcnt(3)
; #define LAS __attribute__((address_space(3)))
; __device__ __forceinline__ void router_tail(const Ctx& F, const float (&lg)[16], const int b, const int t, const bool valid) {
;     const bool b5 = (F.lane & 32) != 0, b4 = (F.lane & 16) != 0, b3 = (F.lane & 8) != 0, b2 = (F.lane & 4) != 0;
;     float r8[8], r4[4], r2[2];
; #pragma unroll
;     for (int e = 0; e < 8; ++e) { const float keep = b5 ? lg[e + 8] : lg[e], send = b5 ? lg[e] : lg[e + 8]; r8[e] = keep + __shfl_xor(send, 32); }
; #pragma unroll
;     for (int e = 0; e < 4; ++e) { const float keep = b4 ? r8[e + 4] : r8[e], send = b4 ? r8[e] : r8[e + 4]; r4[e] = keep + __shfl_xor(send, 16); }
; #pragma unroll
;     for (int e = 0; e < 2; ++e) { const float keep = b3 ? r4[e + 2] : r4[e], send = b3 ? r4[e] : r4[e + 2]; r2[e] = keep + __shfl_xor(send, 8); }
;     float lgt; { const float keep = b2 ? r2[1] : r2[0], send = b2 ? r2[0] : r2[1]; lgt = keep + __shfl_xor(send, 4); }
;     lgt += __shfl_xor(lgt, 2); lgt += __shfl_xor(lgt, 1);
;     float mx = lgt;
;     mx = fmaxf(mx, __shfl_xor(mx, 4)); mx = fmaxf(mx, __shfl_xor(mx, 8)); mx = fmaxf(mx, __shfl_xor(mx, 16)); mx = fmaxf(mx, __shfl_xor(mx, 32));
;     const float ex = expf(lgt - mx); float sum = ex;
;     sum += __shfl_xor(sum, 4); sum += __shfl_xor(sum, 8); sum += __shfl_xor(sum, 16); sum += __shfl_xor(sum, 32);
;     if (valid && (F.lane & 3) == 0) { const float af = ex / sum; const int e = F.lane >> 2;
;         if (t < CTXL) F.affc[((size_t)(b * 16 + e)) * CTXL + t] = af; else F.affl[((size_t)(b * 16 + e)) * SEQ + (t - CTXL)] = af; }
; __device__ __forceinline__ void phase_norm2(const Params& p, const Ctx& F, const int l) {
;     ...
; #pragma unroll
;         for (int e = 0; e < 16; ++e) { f32x2 a = {0.f, 0.f};
; #pragma unroll
;             for (int j = 0; j < 8; ++j) { const f32x4 w = *((const LAS f32x4*)(wr2 + e * DM) + F.lane + 64 * j);
; #pragma unroll
;                 for (int c = 0; c < 4; ++c) a += vv[j][c] * w[c]; }
;             lg[e] = a; }
;         float lg0[16], lg1[16];
; #pragma unroll
;         for (int e = 0; e < 16; ++e) { lg0[e] = lg[e].x; lg1[e] = lg[e].y; }
;         router_tail(F, lg0, b, t, true);
	v_pk_fma_f32 v[108:109], v[108:109], v[232:233], v[118:119] op_sel_hi:[1,0,1]
	s_nop 0
	v_pk_fma_f32 v[108:109], v[110:111], v[232:233], v[108:109] op_sel:[0,1,0]
	v_mov_b32_e32 v110, v235
	v_pk_fma_f32 v[108:109], v[116:117], v[234:235], v[108:109] op_sel_hi:[1,0,1]
	s_nop 0
	v_pk_fma_f32 v[112:113], v[120:121], v[110:111], v[108:109] op_sel_hi:[1,0,1]
	ds_read_b128 v[228:231], v244 offset:63488
	s_waitcnt lgkmcnt(3)
	v_pk_fma_f32 v[96:97], v[96:97], v[236:237], v[112:113] op_sel_hi:[1,0,1]
	s_nop 0
	v_pk_fma_f32 v[96:97], v[98:99], v[236:237], v[96:97] op_sel:[0,1,0]
	v_mov_b32_e32 v98, v239
	v_pk_fma_f32 v[96:97], v[102:103], v[238:239], v[96:97] op_sel_hi:[1,0,1]
	s_nop 0
	v_pk_fma_f32 v[102:103], v[106:107], v[98:99], v[96:97] op_sel_hi:[1,0,1]
	ds_read_b128 v[232:235], v244 offset:64512
	s_waitcnt lgkmcnt(3)
	v_pk_fma_f32 v[92:93], v[92:93], v[240:241], v[102:103] op_sel_hi:[1,0,1]
	s_nop 0
	v_pk_fma_f32 v[92:93], v[94:95], v[240:241], v[92:93] op_sel:[0,1,0]
	v_mov_b32_e32 v94, v243
	v_pk_fma_f32 v[92:93], v[100:101], v[242:243], v[92:93] op_sel_hi:[1,0,1]
	s_nop 0
	v_pk_fma_f32 v[96:97], v[104:105], v[94:95], v[92:93] op_sel_hi:[1,0,1]
	s_waitcnt lgkmcnt(2)
	v_pk_fma_f32 v[80:81], v[80:81], v[224:225], v[96:97] op_sel_hi:[1,0,1]
	s_nop 0
	v_pk_fma_f32 v[80:81], v[82:83], v[224:225], v[80:81] op_sel:[0,1,0]
	v_mov_b32_e32 v82, v227
	v_pk_fma_f32 v[80:81], v[86:87], v[226:227], v[80:81] op_sel_hi:[1,0,1]
	s_nop 0
	v_pk_fma_f32 v[86:87], v[90:91], v[82:83], v[80:81] op_sel_hi:[1,0,1]
	s_waitcnt lgkmcnt(1)
	v_pk_fma_f32 v[76:77], v[76:77], v[228:229], v[86:87] op_sel_hi:[1,0,1]
	s_nop 0
	v_pk_fma_f32 v[76:77], v[78:79], v[228:229], v[76:77] op_sel:[0,1,0]
	v_mov_b32_e32 v78, v231
	v_pk_fma_f32 v[76:77], v[84:85], v[230:231], v[76:77] op_sel_hi:[1,0,1]
	s_nop 0
	v_pk_fma_f32 v[80:81], v[88:89], v[78:79], v[76:77] op_sel_hi:[1,0,1]
	v_cndmask_b32_e64 v1, v168, v152, s[38:39]
	s_waitcnt lgkmcnt(0)
	v_pk_fma_f32 v[68:69], v[68:69], v[232:233], v[80:81] op_sel_hi:[1,0,1]
	s_nop 0
	v_pk_fma_f32 v[68:69], v[70:71], v[232:233], v[68:69] op_sel:[0,1,0]
	v_mov_b32_e32 v70, v235
	v_pk_fma_f32 v[68:69], v[72:73], v[234:235], v[68:69] op_sel_hi:[1,0,1]
	v_cndmask_b32_e64 v72, v156, v172, s[38:39]
	v_pk_fma_f32 v[68:69], v[74:75], v[70:71], v[68:69] op_sel_hi:[1,0,1]
	v_cndmask_b32_e64 v70, v152, v168, s[38:39]
	ds_bpermute_b32 v70, v194, v70
	v_cndmask_b32_e64 v71, v154, v170, s[38:39]
	ds_bpermute_b32 v71, v194, v71
	ds_bpermute_b32 v72, v194, v72
	v_cndmask_b32_e64 v73, v158, v174, s[38:39]
	ds_bpermute_b32 v73, v194, v73
	v_cndmask_b32_e64 v74, v160, v176, s[38:39]
	ds_bpermute_b32 v74, v194, v74
	v_cndmask_b32_e64 v75, v162, v178, s[38:39]
	s_waitcnt lgkmcnt(4)
	v_add_f32_e32 v1, v1, v70
	v_cndmask_b32_e64 v70, v170, v154, s[38:39]
	ds_bpermute_b32 v75, v194, v75
	v_cndmask_b32_e64 v76, v164, v180, s[38:39]
	s_waitcnt lgkmcnt(4)
	v_add_f32_e32 v70, v70, v71
	v_cndmask_b32_e64 v71, v172, v156, s[38:39]
	ds_bpermute_b32 v76, v194, v76
	s_waitcnt lgkmcnt(4)
	v_add_f32_e32 v71, v71, v72
	v_cndmask_b32_e64 v72, v174, v158, s[38:39]
	s_waitcnt lgkmcnt(3)
	v_add_f32_e32 v72, v72, v73
	v_cndmask_b32_e64 v73, v176, v160, s[38:39]
	s_waitcnt lgkmcnt(2)
	v_add_f32_e32 v73, v73, v74
	v_cndmask_b32_e64 v74, v178, v162, s[38:39]
	s_waitcnt lgkmcnt(1)
	v_add_f32_e32 v74, v74, v75
	v_cndmask_b32_e64 v75, v180, v164, s[38:39]
	s_waitcnt lgkmcnt(0)
	v_add_f32_e32 v75, v75, v76
	v_cndmask_b32_e64 v76, v68, v166, s[38:39]
	v_cndmask_b32_e64 v68, v166, v68, s[38:39]
	ds_bpermute_b32 v68, v194, v68
	s_waitcnt lgkmcnt(0)
	v_add_f32_e32 v68, v76, v68
	v_cndmask_b32_e64 v76, v73, v1, s[40:41]
	v_cndmask_b32_e64 v1, v1, v73, s[40:41]
	v_cndmask_b32_e64 v73, v74, v70, s[40:41]
	v_cndmask_b32_e64 v70, v70, v74, s[40:41]
	ds_bpermute_b32 v70, v193, v70
	ds_bpermute_b32 v1, v193, v1
	s_waitcnt lgkmcnt(1)
	v_add_f32_e32 v70, v73, v70
	v_cndmask_b32_e64 v73, v75, v71, s[40:41]
	v_cndmask_b32_e64 v71, v71, v75, s[40:41]
	ds_bpermute_b32 v71, v193, v71
	s_waitcnt lgkmcnt(1)
	v_add_f32_e32 v1, v76, v1
	s_waitcnt lgkmcnt(0)
	v_add_f32_e32 v71, v73, v71
	v_cndmask_b32_e64 v73, v68, v72, s[40:41]
	v_cndmask_b32_e64 v68, v72, v68, s[40:41]
	ds_bpermute_b32 v68, v193, v68
	v_cndmask_b32_e64 v72, v71, v1, s[42:43]
	v_cndmask_b32_e64 v1, v1, v71, s[42:43]
	ds_bpermute_b32 v1, v192, v1
	s_waitcnt lgkmcnt(1)
	v_add_f32_e32 v68, v73, v68
	v_cndmask_b32_e64 v71, v68, v70, s[42:43]
	v_cndmask_b32_e64 v68, v70, v68, s[42:43]
	ds_bpermute_b32 v68, v192, v68
	s_waitcnt lgkmcnt(1)
	v_add_f32_e32 v1, v72, v1
	s_waitcnt lgkmcnt(0)
	v_add_f32_e32 v68, v71, v68
	v_cndmask_b32_e64 v70, v68, v1, s[4:5]
	v_cndmask_b32_e64 v1, v1, v68, s[4:5]
	ds_bpermute_b32 v1, v191, v1
	s_waitcnt lgkmcnt(0)
	v_add_f32_e32 v1, v70, v1
	ds_bpermute_b32 v68, v190, v1
	s_waitcnt lgkmcnt(0)
	v_add_f32_e32 v1, v1, v68
	ds_bpermute_b32 v68, v133, v1
	s_waitcnt lgkmcnt(0)
	v_add_f32_e32 v1, v1, v68
	ds_bpermute_b32 v68, v191, v1
	s_waitcnt lgkmcnt(0)
	v_max_f32_e32 v68, v68, v68
	v_max_f32_e32 v68, v1, v68
	ds_bpermute_b32 v70, v192, v68
	s_waitcnt lgkmcnt(0)
	v_max_f32_e32 v70, v70, v70
	v_max_f32_e32 v68, v68, v70
	ds_bpermute_b32 v70, v193, v68
	s_waitcnt lgkmcnt(0)
	v_max_f32_e32 v70, v70, v70
	v_max_f32_e32 v68, v68, v70
	ds_bpermute_b32 v70, v194, v68
	s_waitcnt lgkmcnt(0)
	v_max_f32_e32 v70, v70, v70
	v_max_f32_e32 v68, v68, v70
	v_sub_f32_e32 v1, v1, v68
	v_mul_f32_e32 v68, 0x3fb8aa3b, v1
	v_fma_f32 v70, v1, s55, -v68
	v_rndne_f32_e32 v71, v68
	v_fmac_f32_e32 v70, 0x32a5705f, v1
	v_sub_f32_e32 v68, v68, v71
	v_add_f32_e32 v68, v68, v70
	v_exp_f32_e32 v68, v68
	v_cvt_i32_f32_e32 v70, v71
	v_cmp_ngt_f32_e32 vcc, s56, v1
	v_ldexp_f32 v68, v68, v70
	s_nop 0
	v_cndmask_b32_e32 v68, 0, v68, vcc
	v_cmp_nlt_f32_e32 vcc, s57, v1
	s_nop 1
	v_cndmask_b32_e32 v68, v222, v68, vcc
	ds_bpermute_b32 v1, v191, v68
	s_waitcnt lgkmcnt(0)
	v_add_f32_e32 v1, v68, v1
	ds_bpermute_b32 v70, v192, v1
	s_waitcnt lgkmcnt(0)
	v_add_f32_e32 v1, v1, v70
	ds_bpermute_b32 v70, v193, v1
	s_waitcnt lgkmcnt(0)
	v_add_f32_e32 v70, v1, v70
	ds_bpermute_b32 v71, v194, v70
	s_and_saveexec_b64 s[0:1], s[6:7]
	s_cbranch_execz .LBB0_942
	s_waitcnt lgkmcnt(0)
	v_add_f32_e32 v1, v70, v71
	v_div_scale_f32 v70, s[12:13], v1, v1, v68
	v_rcp_f32_e32 v71, v70
	v_div_scale_f32 v72, vcc, v68, v1, v68
	s_cmpk_gt_i32 s60, 0xff
	v_fma_f32 v73, -v70, v71, 1.0
	v_fmac_f32_e32 v71, v73, v71
	v_mul_f32_e32 v73, v72, v71
	v_fma_f32 v74, -v70, v73, v72
	v_fmac_f32_e32 v73, v74, v71
	v_fma_f32 v70, -v70, v73, v72
	v_div_fmas_f32 v70, v70, v71, v73
	v_div_fixup_f32 v68, v70, v1, v68
	s_mov_b64 s[12:13], -1
	s_cbranch_scc0 .LBB0_940
	v_lshl_add_u64 v[70:71], s[60:61], 2, v[148:149]
	global_store_dword v[70:71], v68, off offset:-1024
	s_mov_b64 s[12:13], 0
